# GEMM K-loop: last LDS-DMA of the 6-DMA stage segment issued at the head of the next read segment (5/3 instead of 6/2), vmcnt 8->7
# speedup vs baseline: 1.0306x; 1.0002x over previous
.LBB0_144:
	s_add_u32 s40, s14, 0x80
	s_addc_u32 s41, s15, 0
	s_waitcnt vmcnt(8)
	s_and_b64 s[38:39], s[38:39], exec
	s_waitcnt lgkmcnt(0)
	s_cselect_b32 s38, s13, s60
	s_cselect_b32 s43, s31, s41
	s_cselect_b32 s42, s30, s40
	s_cselect_b32 s39, s9, s61
	s_add_u32 s40, s38, 0x8000
	s_addc_u32 s41, s39, 0
	s_barrier
	s_setprio 1
	s_waitcnt lgkmcnt(0)
	v_mfma_f32_16x16x32_bf16 v[132:135], v[152:155], v[192:195], v[132:135]
	v_mfma_f32_16x16x32_bf16 v[128:131], v[160:163], v[192:195], v[128:131]
	v_mfma_f32_16x16x32_bf16 v[124:127], v[152:155], v[184:187], v[124:127]
	v_mfma_f32_16x16x32_bf16 v[116:119], v[160:163], v[184:187], v[116:119]
	v_mfma_f32_16x16x32_bf16 v[108:111], v[152:155], v[176:179], v[108:111]
	v_mfma_f32_16x16x32_bf16 v[100:103], v[160:163], v[176:179], v[100:103]
	v_mfma_f32_16x16x32_bf16 v[92:95], v[152:155], v[168:171], v[92:95]
	v_mfma_f32_16x16x32_bf16 v[80:83], v[160:163], v[168:171], v[80:83]
	v_mfma_f32_16x16x32_bf16 v[132:135], v[156:159], v[196:199], v[132:135]
	v_mfma_f32_16x16x32_bf16 v[128:131], v[164:167], v[196:199], v[128:131]
	v_mfma_f32_16x16x32_bf16 v[124:127], v[156:159], v[188:191], v[124:127]
	v_mfma_f32_16x16x32_bf16 v[116:119], v[164:167], v[188:191], v[116:119]
	v_mfma_f32_16x16x32_bf16 v[108:111], v[156:159], v[180:183], v[108:111]
	v_mfma_f32_16x16x32_bf16 v[100:103], v[164:167], v[180:183], v[100:103]
	v_mfma_f32_16x16x32_bf16 v[92:95], v[156:159], v[172:175], v[92:95]
	v_mfma_f32_16x16x32_bf16 v[80:83], v[164:167], v[172:175], v[80:83]
	s_setprio 0
	s_setprio 1
	v_mfma_f32_16x16x32_bf16 v[120:123], v[136:139], v[192:195], v[120:123]
	v_mfma_f32_16x16x32_bf16 v[112:115], v[144:147], v[192:195], v[112:115]
	v_mfma_f32_16x16x32_bf16 v[104:107], v[136:139], v[184:187], v[104:107]
	v_mfma_f32_16x16x32_bf16 v[96:99], v[144:147], v[184:187], v[96:99]
	v_mfma_f32_16x16x32_bf16 v[88:91], v[136:139], v[176:179], v[88:91]
	v_mfma_f32_16x16x32_bf16 v[76:79], v[144:147], v[176:179], v[76:79]
	v_mfma_f32_16x16x32_bf16 v[72:75], v[136:139], v[168:171], v[72:75]
	v_mfma_f32_16x16x32_bf16 v[68:71], v[144:147], v[168:171], v[68:71]
	v_mfma_f32_16x16x32_bf16 v[120:123], v[140:143], v[196:199], v[120:123]
	v_mfma_f32_16x16x32_bf16 v[112:115], v[148:151], v[196:199], v[112:115]
	v_mfma_f32_16x16x32_bf16 v[104:107], v[140:143], v[188:191], v[104:107]
	v_mfma_f32_16x16x32_bf16 v[96:99], v[148:151], v[188:191], v[96:99]
	v_mfma_f32_16x16x32_bf16 v[88:91], v[140:143], v[180:183], v[88:91]
	v_mfma_f32_16x16x32_bf16 v[76:79], v[148:151], v[180:183], v[76:79]
	v_mfma_f32_16x16x32_bf16 v[72:75], v[140:143], v[172:175], v[72:75]
	v_mfma_f32_16x16x32_bf16 v[68:71], v[148:151], v[172:175], v[68:71]
	s_setprio 0
	s_barrier
	s_mov_b32 m0, s48
	v_lshl_add_u64 v[204:205], s[38:39], 0, v[210:211]
	s_add_u32 s64, s38, 0x4000
	ds_read_b128 v[168:171], v244 offset:16384
	ds_read_b128 v[172:175], v244 offset:17408
	ds_read_b128 v[176:179], v244 offset:18432
	ds_read_b128 v[180:183], v244 offset:19456
	ds_read_b128 v[184:187], v244 offset:20480
	ds_read_b128 v[188:191], v244 offset:21504
	ds_read_b128 v[192:195], v244 offset:22528
	ds_read_b128 v[196:199], v244 offset:23552
	global_load_lds_dwordx4 v[204:205], off
	v_lshl_add_u64 v[204:205], s[38:39], 0, v[208:209]
	s_mov_b32 m0, s49
	s_addc_u32 s65, s39, 0
	global_load_lds_dwordx4 v[204:205], off
	v_lshl_add_u64 v[204:205], s[64:65], 0, v[210:211]
	s_mov_b32 m0, s50
	v_mov_b32_e32 v215, v3
	global_load_lds_dwordx4 v[204:205], off
	v_lshl_add_u64 v[204:205], s[64:65], 0, v[208:209]
	s_mov_b32 m0, s51
	v_lshl_add_u64 v[248:249], s[42:43], 0, v[214:215]
	global_load_lds_dwordx4 v[204:205], off
	s_mov_b32 m0, s47
	v_lshl_add_u64 v[204:205], s[42:43], 0, v[2:3]
	global_load_lds_dwordx4 v2, s[42:43]
	s_waitcnt vmcnt(7)
	s_waitcnt lgkmcnt(0)
	s_barrier
	s_setprio 1
	s_waitcnt lgkmcnt(0)
	v_mfma_f32_16x16x32_bf16 v[64:67], v[152:155], v[168:171], v[64:67]
	v_mfma_f32_16x16x32_bf16 v[60:63], v[160:163], v[168:171], v[60:63]
	v_mfma_f32_16x16x32_bf16 v[56:59], v[152:155], v[176:179], v[56:59]
	v_mfma_f32_16x16x32_bf16 v[48:51], v[160:163], v[176:179], v[48:51]
	v_mfma_f32_16x16x32_bf16 v[40:43], v[152:155], v[184:187], v[40:43]
	v_mfma_f32_16x16x32_bf16 v[32:35], v[160:163], v[184:187], v[32:35]
	v_mfma_f32_16x16x32_bf16 v[24:27], v[152:155], v[192:195], v[24:27]
	v_mfma_f32_16x16x32_bf16 v[16:19], v[160:163], v[192:195], v[16:19]
	v_mfma_f32_16x16x32_bf16 v[64:67], v[156:159], v[172:175], v[64:67]
	v_mfma_f32_16x16x32_bf16 v[60:63], v[164:167], v[172:175], v[60:63]
	v_mfma_f32_16x16x32_bf16 v[56:59], v[156:159], v[180:183], v[56:59]
	v_mfma_f32_16x16x32_bf16 v[48:51], v[164:167], v[180:183], v[48:51]
	v_mfma_f32_16x16x32_bf16 v[40:43], v[156:159], v[188:191], v[40:43]
	v_mfma_f32_16x16x32_bf16 v[32:35], v[164:167], v[188:191], v[32:35]
	v_mfma_f32_16x16x32_bf16 v[24:27], v[156:159], v[196:199], v[24:27]
	v_mfma_f32_16x16x32_bf16 v[16:19], v[164:167], v[196:199], v[16:19]
	s_setprio 0
	s_setprio 1
	v_mfma_f32_16x16x32_bf16 v[52:55], v[136:139], v[168:171], v[52:55]
	v_mfma_f32_16x16x32_bf16 v[44:47], v[144:147], v[168:171], v[44:47]
	v_mfma_f32_16x16x32_bf16 v[36:39], v[136:139], v[176:179], v[36:39]
	v_mfma_f32_16x16x32_bf16 v[28:31], v[144:147], v[176:179], v[28:31]
	v_mfma_f32_16x16x32_bf16 v[20:23], v[136:139], v[184:187], v[20:23]
	v_mfma_f32_16x16x32_bf16 v[12:15], v[144:147], v[184:187], v[12:15]
	v_mfma_f32_16x16x32_bf16 v[8:11], v[136:139], v[192:195], v[8:11]
	v_mfma_f32_16x16x32_bf16 v[4:7], v[144:147], v[192:195], v[4:7]
	v_mfma_f32_16x16x32_bf16 v[52:55], v[140:143], v[172:175], v[52:55]
	v_mfma_f32_16x16x32_bf16 v[44:47], v[148:151], v[172:175], v[44:47]
	v_mfma_f32_16x16x32_bf16 v[36:39], v[140:143], v[180:183], v[36:39]
	v_mfma_f32_16x16x32_bf16 v[28:31], v[148:151], v[180:183], v[28:31]
	v_mfma_f32_16x16x32_bf16 v[20:23], v[140:143], v[188:191], v[20:23]
	v_mfma_f32_16x16x32_bf16 v[12:15], v[148:151], v[188:191], v[12:15]
	v_mfma_f32_16x16x32_bf16 v[8:11], v[140:143], v[196:199], v[8:11]
	v_mfma_f32_16x16x32_bf16 v[4:7], v[148:151], v[196:199], v[4:7]
	s_setprio 0
	s_barrier
	s_mov_b32 m0, s52
	s_nop 0
	global_load_lds_dwordx4 v214, s[42:43]
	s_add_i32 s63, 0, 0x18000
	s_add_i32 s64, 0, 0x1c000
	v_add_u32_e32 v148, s63, v243
	v_add_u32_e32 v164, s64, v243
	ds_read_b128 v[136:139], v148
	ds_read_b128 v[140:143], v148 offset:1024
	ds_read_b128 v[144:147], v148 offset:2048
	ds_read_b128 v[148:151], v148 offset:3072
	ds_read_b128 v[152:155], v164
	ds_read_b128 v[156:159], v164 offset:1024
	ds_read_b128 v[160:163], v164 offset:2048
	ds_read_b128 v[164:167], v164 offset:3072
	s_mov_b32 m0, s53
	v_lshl_add_u64 v[226:227], s[42:43], 0, v[226:227]
	ds_read_b128 v[168:171], v244 offset:32768
	ds_read_b128 v[172:175], v244 offset:33792
	ds_read_b128 v[176:179], v244 offset:34816
	ds_read_b128 v[180:183], v244 offset:35840
	ds_read_b128 v[184:187], v244 offset:36864
	ds_read_b128 v[188:191], v244 offset:37888
	ds_read_b128 v[192:195], v244 offset:38912
	ds_read_b128 v[196:199], v244 offset:39936
	global_load_lds_dwordx4 v[226:227], off
	v_lshl_add_u64 v[224:225], s[42:43], 0, v[224:225]
	s_mov_b32 m0, s54
	s_nop 0
	global_load_lds_dwordx4 v[224:225], off
	s_waitcnt vmcnt(8)
	s_waitcnt lgkmcnt(0)
	s_barrier
	s_setprio 1
	s_waitcnt lgkmcnt(0)
	v_mfma_f32_16x16x32_bf16 v[132:135], v[136:139], v[168:171], v[132:135]
	v_mfma_f32_16x16x32_bf16 v[128:131], v[144:147], v[168:171], v[128:131]
	v_mfma_f32_16x16x32_bf16 v[124:127], v[136:139], v[176:179], v[124:127]
	v_mfma_f32_16x16x32_bf16 v[116:119], v[144:147], v[176:179], v[116:119]
	v_mfma_f32_16x16x32_bf16 v[108:111], v[136:139], v[184:187], v[108:111]
	v_mfma_f32_16x16x32_bf16 v[100:103], v[144:147], v[184:187], v[100:103]
	v_mfma_f32_16x16x32_bf16 v[92:95], v[136:139], v[192:195], v[92:95]
	v_mfma_f32_16x16x32_bf16 v[80:83], v[144:147], v[192:195], v[80:83]
	v_mfma_f32_16x16x32_bf16 v[132:135], v[140:143], v[172:175], v[132:135]
	v_mfma_f32_16x16x32_bf16 v[128:131], v[148:151], v[172:175], v[128:131]
	v_mfma_f32_16x16x32_bf16 v[124:127], v[140:143], v[180:183], v[124:127]
	v_mfma_f32_16x16x32_bf16 v[116:119], v[148:151], v[180:183], v[116:119]
	v_mfma_f32_16x16x32_bf16 v[108:111], v[140:143], v[188:191], v[108:111]
	v_mfma_f32_16x16x32_bf16 v[100:103], v[148:151], v[188:191], v[100:103]
	v_mfma_f32_16x16x32_bf16 v[92:95], v[140:143], v[196:199], v[92:95]
	v_mfma_f32_16x16x32_bf16 v[80:83], v[148:151], v[196:199], v[80:83]
	s_setprio 0
	s_setprio 1
	v_mfma_f32_16x16x32_bf16 v[120:123], v[152:155], v[168:171], v[120:123]
	v_mfma_f32_16x16x32_bf16 v[112:115], v[160:163], v[168:171], v[112:115]
	v_mfma_f32_16x16x32_bf16 v[104:107], v[152:155], v[176:179], v[104:107]
	v_mfma_f32_16x16x32_bf16 v[96:99], v[160:163], v[176:179], v[96:99]
	v_mfma_f32_16x16x32_bf16 v[88:91], v[152:155], v[184:187], v[88:91]
	v_mfma_f32_16x16x32_bf16 v[76:79], v[160:163], v[184:187], v[76:79]
	v_mfma_f32_16x16x32_bf16 v[72:75], v[152:155], v[192:195], v[72:75]
	v_mfma_f32_16x16x32_bf16 v[68:71], v[160:163], v[192:195], v[68:71]
	v_mfma_f32_16x16x32_bf16 v[120:123], v[156:159], v[172:175], v[120:123]
	v_mfma_f32_16x16x32_bf16 v[112:115], v[164:167], v[172:175], v[112:115]
	v_mfma_f32_16x16x32_bf16 v[104:107], v[156:159], v[180:183], v[104:107]
	v_mfma_f32_16x16x32_bf16 v[96:99], v[164:167], v[180:183], v[96:99]
	v_mfma_f32_16x16x32_bf16 v[88:91], v[156:159], v[188:191], v[88:91]
	v_mfma_f32_16x16x32_bf16 v[76:79], v[164:167], v[188:191], v[76:79]
	v_mfma_f32_16x16x32_bf16 v[72:75], v[156:159], v[196:199], v[72:75]
	v_mfma_f32_16x16x32_bf16 v[68:71], v[164:167], v[196:199], v[68:71]
	s_setprio 0
	s_barrier
	s_add_i32 s42, s63, s45
	v_lshl_add_u64 v[224:225], s[40:41], 0, v[210:211]
	s_mov_b32 m0, s42
	ds_read_b128 v[168:171], v244 offset:49152
	ds_read_b128 v[172:175], v244 offset:50176
	ds_read_b128 v[176:179], v244 offset:51200
	ds_read_b128 v[180:183], v244 offset:52224
	ds_read_b128 v[184:187], v244 offset:53248
	ds_read_b128 v[188:191], v244 offset:54272
	ds_read_b128 v[192:195], v244 offset:55296
	ds_read_b128 v[196:199], v244 offset:56320
	global_load_lds_dwordx4 v[224:225], off
	s_add_i32 m0, s42, 0x2000
	s_add_u32 s38, s38, 0xc000
	v_lshl_add_u64 v[224:225], s[40:41], 0, v[208:209]
	s_addc_u32 s39, s39, 0
	s_add_i32 s40, s64, s45
	global_load_lds_dwordx4 v[224:225], off
	v_lshl_add_u64 v[224:225], s[38:39], 0, v[210:211]
	s_mov_b32 m0, s40
	v_lshl_add_u64 v[204:205], v[204:205], 0, s[36:37]
	global_load_lds_dwordx4 v[224:225], off
	v_lshl_add_u64 v[224:225], s[38:39], 0, v[208:209]
	s_add_i32 m0, s40, 0x2000
	s_nop 0
	global_load_lds_dwordx4 v[224:225], off
	s_mov_b32 m0, s55
	s_nop 0
	global_load_lds_dwordx4 v[204:205], off
	v_lshl_add_u64 v[204:205], v[248:249], 0, s[36:37]
	s_mov_b32 m0, s56
	s_nop 0
	global_load_lds_dwordx4 v[204:205], off
	s_waitcnt vmcnt(8)
	s_waitcnt lgkmcnt(0)
	s_barrier
	s_setprio 1
	s_waitcnt lgkmcnt(0)
	v_mfma_f32_16x16x32_bf16 v[64:67], v[136:139], v[168:171], v[64:67]
	v_mfma_f32_16x16x32_bf16 v[60:63], v[144:147], v[168:171], v[60:63]
	v_mfma_f32_16x16x32_bf16 v[56:59], v[136:139], v[176:179], v[56:59]
	v_mfma_f32_16x16x32_bf16 v[48:51], v[144:147], v[176:179], v[48:51]
	v_mfma_f32_16x16x32_bf16 v[40:43], v[136:139], v[184:187], v[40:43]
	v_mfma_f32_16x16x32_bf16 v[32:35], v[144:147], v[184:187], v[32:35]
	v_mfma_f32_16x16x32_bf16 v[24:27], v[136:139], v[192:195], v[24:27]
	v_mfma_f32_16x16x32_bf16 v[16:19], v[144:147], v[192:195], v[16:19]
	v_mfma_f32_16x16x32_bf16 v[64:67], v[140:143], v[172:175], v[64:67]
	v_mfma_f32_16x16x32_bf16 v[60:63], v[148:151], v[172:175], v[60:63]
	v_mfma_f32_16x16x32_bf16 v[56:59], v[140:143], v[180:183], v[56:59]
	v_mfma_f32_16x16x32_bf16 v[48:51], v[148:151], v[180:183], v[48:51]
	v_mfma_f32_16x16x32_bf16 v[40:43], v[140:143], v[188:191], v[40:43]
	v_mfma_f32_16x16x32_bf16 v[32:35], v[148:151], v[188:191], v[32:35]
	v_mfma_f32_16x16x32_bf16 v[24:27], v[140:143], v[196:199], v[24:27]
	v_mfma_f32_16x16x32_bf16 v[16:19], v[148:151], v[196:199], v[16:19]
	s_setprio 0
	s_setprio 1
	v_mfma_f32_16x16x32_bf16 v[52:55], v[152:155], v[168:171], v[52:55]
	v_mfma_f32_16x16x32_bf16 v[44:47], v[160:163], v[168:171], v[44:47]
	v_mfma_f32_16x16x32_bf16 v[36:39], v[152:155], v[176:179], v[36:39]
	v_mfma_f32_16x16x32_bf16 v[28:31], v[160:163], v[176:179], v[28:31]
	v_mfma_f32_16x16x32_bf16 v[20:23], v[152:155], v[184:187], v[20:23]
	v_mfma_f32_16x16x32_bf16 v[12:15], v[160:163], v[184:187], v[12:15]
	v_mfma_f32_16x16x32_bf16 v[8:11], v[152:155], v[192:195], v[8:11]
	v_mfma_f32_16x16x32_bf16 v[4:7], v[160:163], v[192:195], v[4:7]
	v_mfma_f32_16x16x32_bf16 v[52:55], v[156:159], v[172:175], v[52:55]
	v_mfma_f32_16x16x32_bf16 v[44:47], v[164:167], v[172:175], v[44:47]
	v_mfma_f32_16x16x32_bf16 v[36:39], v[156:159], v[180:183], v[36:39]
	v_mfma_f32_16x16x32_bf16 v[28:31], v[164:167], v[180:183], v[28:31]
	v_mfma_f32_16x16x32_bf16 v[20:23], v[156:159], v[188:191], v[20:23]
	v_mfma_f32_16x16x32_bf16 v[12:15], v[164:167], v[188:191], v[12:15]
	v_mfma_f32_16x16x32_bf16 v[8:11], v[156:159], v[196:199], v[8:11]
	v_mfma_f32_16x16x32_bf16 v[4:7], v[164:167], v[196:199], v[4:7]
	s_setprio 0
	s_barrier
	s_add_i32 s62, s62, 2
	s_add_u32 s60, s60, 0x10000
	s_addc_u32 s61, s61, 0
	s_add_u32 s14, s14, 0x100
	s_addc_u32 s15, s15, 0
	s_cmp_gt_u32 s62, 29
	s_cbranch_scc1 .LBB0_147

.LBB0_294:
	s_add_u32 s40, s14, 0x80
	s_addc_u32 s41, s15, 0
	s_waitcnt vmcnt(8)
	s_and_b64 s[38:39], s[38:39], exec
	s_waitcnt lgkmcnt(0)
	s_cselect_b32 s38, s13, s59
	s_cselect_b32 s43, s1, s41
	s_cselect_b32 s42, s0, s40
	s_cselect_b32 s39, s9, s60
	s_add_u32 s40, s38, 0x8000
	s_addc_u32 s41, s39, 0
	s_barrier
	s_setprio 1
	s_waitcnt lgkmcnt(0)
	v_mfma_f32_16x16x32_bf16 v[132:135], v[152:155], v[192:195], v[132:135]
	v_mfma_f32_16x16x32_bf16 v[128:131], v[160:163], v[192:195], v[128:131]
	v_mfma_f32_16x16x32_bf16 v[124:127], v[152:155], v[184:187], v[124:127]
	v_mfma_f32_16x16x32_bf16 v[120:123], v[160:163], v[184:187], v[120:123]
	v_mfma_f32_16x16x32_bf16 v[108:111], v[152:155], v[176:179], v[108:111]
	v_mfma_f32_16x16x32_bf16 v[104:107], v[160:163], v[176:179], v[104:107]
	v_mfma_f32_16x16x32_bf16 v[92:95], v[152:155], v[168:171], v[92:95]
	v_mfma_f32_16x16x32_bf16 v[88:91], v[160:163], v[168:171], v[88:91]
	v_mfma_f32_16x16x32_bf16 v[132:135], v[156:159], v[196:199], v[132:135]
	v_mfma_f32_16x16x32_bf16 v[128:131], v[164:167], v[196:199], v[128:131]
	v_mfma_f32_16x16x32_bf16 v[124:127], v[156:159], v[188:191], v[124:127]
	v_mfma_f32_16x16x32_bf16 v[120:123], v[164:167], v[188:191], v[120:123]
	v_mfma_f32_16x16x32_bf16 v[108:111], v[156:159], v[180:183], v[108:111]
	v_mfma_f32_16x16x32_bf16 v[104:107], v[164:167], v[180:183], v[104:107]
	v_mfma_f32_16x16x32_bf16 v[92:95], v[156:159], v[172:175], v[92:95]
	v_mfma_f32_16x16x32_bf16 v[88:91], v[164:167], v[172:175], v[88:91]
	s_setprio 0
	s_setprio 1
	v_mfma_f32_16x16x32_bf16 v[116:119], v[136:139], v[192:195], v[116:119]
	v_mfma_f32_16x16x32_bf16 v[112:115], v[144:147], v[192:195], v[112:115]
	v_mfma_f32_16x16x32_bf16 v[100:103], v[136:139], v[184:187], v[100:103]
	v_mfma_f32_16x16x32_bf16 v[96:99], v[144:147], v[184:187], v[96:99]
	v_mfma_f32_16x16x32_bf16 v[80:83], v[136:139], v[176:179], v[80:83]
	v_mfma_f32_16x16x32_bf16 v[76:79], v[144:147], v[176:179], v[76:79]
	v_mfma_f32_16x16x32_bf16 v[72:75], v[136:139], v[168:171], v[72:75]
	v_mfma_f32_16x16x32_bf16 v[68:71], v[144:147], v[168:171], v[68:71]
	v_mfma_f32_16x16x32_bf16 v[116:119], v[140:143], v[196:199], v[116:119]
	v_mfma_f32_16x16x32_bf16 v[112:115], v[148:151], v[196:199], v[112:115]
	v_mfma_f32_16x16x32_bf16 v[100:103], v[140:143], v[188:191], v[100:103]
	v_mfma_f32_16x16x32_bf16 v[96:99], v[148:151], v[188:191], v[96:99]
	v_mfma_f32_16x16x32_bf16 v[80:83], v[140:143], v[180:183], v[80:83]
	v_mfma_f32_16x16x32_bf16 v[76:79], v[148:151], v[180:183], v[76:79]
	v_mfma_f32_16x16x32_bf16 v[72:75], v[140:143], v[172:175], v[72:75]
	v_mfma_f32_16x16x32_bf16 v[68:71], v[148:151], v[172:175], v[68:71]
	s_setprio 0
	s_barrier
	s_mov_b32 m0, s47
	v_lshl_add_u64 v[204:205], s[38:39], 0, v[210:211]
	s_add_u32 s62, s38, 0x4000
	ds_read_b128 v[168:171], v244 offset:16384
	ds_read_b128 v[172:175], v244 offset:17408
	ds_read_b128 v[176:179], v244 offset:18432
	ds_read_b128 v[180:183], v244 offset:19456
	ds_read_b128 v[184:187], v244 offset:20480
	ds_read_b128 v[188:191], v244 offset:21504
	ds_read_b128 v[192:195], v244 offset:22528
	ds_read_b128 v[196:199], v244 offset:23552
	global_load_lds_dwordx4 v[204:205], off
	v_lshl_add_u64 v[204:205], s[38:39], 0, v[208:209]
	s_mov_b32 m0, s48
	s_addc_u32 s63, s39, 0
	global_load_lds_dwordx4 v[204:205], off
	v_lshl_add_u64 v[204:205], s[62:63], 0, v[210:211]
	s_mov_b32 m0, s49
	v_mov_b32_e32 v215, v3
	global_load_lds_dwordx4 v[204:205], off
	v_lshl_add_u64 v[204:205], s[62:63], 0, v[208:209]
	s_mov_b32 m0, s50
	v_lshl_add_u64 v[248:249], s[42:43], 0, v[214:215]
	global_load_lds_dwordx4 v[204:205], off
	s_mov_b32 m0, s45
	v_lshl_add_u64 v[204:205], s[42:43], 0, v[2:3]
	global_load_lds_dwordx4 v2, s[42:43]
	s_waitcnt vmcnt(7)
	s_waitcnt lgkmcnt(0)
	s_barrier
	s_setprio 1
	s_waitcnt lgkmcnt(0)
	v_mfma_f32_16x16x32_bf16 v[64:67], v[152:155], v[168:171], v[64:67]
	v_mfma_f32_16x16x32_bf16 v[60:63], v[160:163], v[168:171], v[60:63]
	v_mfma_f32_16x16x32_bf16 v[56:59], v[152:155], v[176:179], v[56:59]
	v_mfma_f32_16x16x32_bf16 v[52:55], v[160:163], v[176:179], v[52:55]
	v_mfma_f32_16x16x32_bf16 v[40:43], v[152:155], v[184:187], v[40:43]
	v_mfma_f32_16x16x32_bf16 v[36:39], v[160:163], v[184:187], v[36:39]
	v_mfma_f32_16x16x32_bf16 v[24:27], v[152:155], v[192:195], v[24:27]
	v_mfma_f32_16x16x32_bf16 v[20:23], v[160:163], v[192:195], v[20:23]
	v_mfma_f32_16x16x32_bf16 v[64:67], v[156:159], v[172:175], v[64:67]
	v_mfma_f32_16x16x32_bf16 v[60:63], v[164:167], v[172:175], v[60:63]
	v_mfma_f32_16x16x32_bf16 v[56:59], v[156:159], v[180:183], v[56:59]
	v_mfma_f32_16x16x32_bf16 v[52:55], v[164:167], v[180:183], v[52:55]
	v_mfma_f32_16x16x32_bf16 v[40:43], v[156:159], v[188:191], v[40:43]
	v_mfma_f32_16x16x32_bf16 v[36:39], v[164:167], v[188:191], v[36:39]
	v_mfma_f32_16x16x32_bf16 v[24:27], v[156:159], v[196:199], v[24:27]
	v_mfma_f32_16x16x32_bf16 v[20:23], v[164:167], v[196:199], v[20:23]
	s_setprio 0
	s_setprio 1
	v_mfma_f32_16x16x32_bf16 v[48:51], v[136:139], v[168:171], v[48:51]
	v_mfma_f32_16x16x32_bf16 v[44:47], v[144:147], v[168:171], v[44:47]
	v_mfma_f32_16x16x32_bf16 v[32:35], v[136:139], v[176:179], v[32:35]
	v_mfma_f32_16x16x32_bf16 v[28:31], v[144:147], v[176:179], v[28:31]
	v_mfma_f32_16x16x32_bf16 v[16:19], v[136:139], v[184:187], v[16:19]
	v_mfma_f32_16x16x32_bf16 v[12:15], v[144:147], v[184:187], v[12:15]
	v_mfma_f32_16x16x32_bf16 v[8:11], v[136:139], v[192:195], v[8:11]
	v_mfma_f32_16x16x32_bf16 v[4:7], v[144:147], v[192:195], v[4:7]
	v_mfma_f32_16x16x32_bf16 v[48:51], v[140:143], v[172:175], v[48:51]
	v_mfma_f32_16x16x32_bf16 v[44:47], v[148:151], v[172:175], v[44:47]
	v_mfma_f32_16x16x32_bf16 v[32:35], v[140:143], v[180:183], v[32:35]
	v_mfma_f32_16x16x32_bf16 v[28:31], v[148:151], v[180:183], v[28:31]
	v_mfma_f32_16x16x32_bf16 v[16:19], v[140:143], v[188:191], v[16:19]
	v_mfma_f32_16x16x32_bf16 v[12:15], v[148:151], v[188:191], v[12:15]
	v_mfma_f32_16x16x32_bf16 v[8:11], v[140:143], v[196:199], v[8:11]
	v_mfma_f32_16x16x32_bf16 v[4:7], v[148:151], v[196:199], v[4:7]
	s_setprio 0
	s_barrier
	s_mov_b32 m0, s51
	s_nop 0
	global_load_lds_dwordx4 v214, s[42:43]
	s_add_i32 s62, 0, 0x18000
	s_add_i32 s63, 0, 0x1c000
	v_add_u32_e32 v148, s62, v243
	v_add_u32_e32 v164, s63, v243
	ds_read_b128 v[136:139], v148
	ds_read_b128 v[140:143], v148 offset:1024
	ds_read_b128 v[144:147], v148 offset:2048
	ds_read_b128 v[148:151], v148 offset:3072
	ds_read_b128 v[152:155], v164
	ds_read_b128 v[156:159], v164 offset:1024
	ds_read_b128 v[160:163], v164 offset:2048
	ds_read_b128 v[164:167], v164 offset:3072
	s_mov_b32 m0, s52
	v_lshl_add_u64 v[226:227], s[42:43], 0, v[226:227]
	ds_read_b128 v[168:171], v244 offset:32768
	ds_read_b128 v[172:175], v244 offset:33792
	ds_read_b128 v[176:179], v244 offset:34816
	ds_read_b128 v[180:183], v244 offset:35840
	ds_read_b128 v[184:187], v244 offset:36864
	ds_read_b128 v[188:191], v244 offset:37888
	ds_read_b128 v[192:195], v244 offset:38912
	ds_read_b128 v[196:199], v244 offset:39936
	global_load_lds_dwordx4 v[226:227], off
	v_lshl_add_u64 v[224:225], s[42:43], 0, v[224:225]
	s_mov_b32 m0, s53
	s_nop 0
	global_load_lds_dwordx4 v[224:225], off
	s_waitcnt vmcnt(8)
	s_waitcnt lgkmcnt(0)
	s_barrier
	s_setprio 1
	s_waitcnt lgkmcnt(0)
	v_mfma_f32_16x16x32_bf16 v[132:135], v[136:139], v[168:171], v[132:135]
	v_mfma_f32_16x16x32_bf16 v[128:131], v[144:147], v[168:171], v[128:131]
	v_mfma_f32_16x16x32_bf16 v[124:127], v[136:139], v[176:179], v[124:127]
	v_mfma_f32_16x16x32_bf16 v[120:123], v[144:147], v[176:179], v[120:123]
	v_mfma_f32_16x16x32_bf16 v[108:111], v[136:139], v[184:187], v[108:111]
	v_mfma_f32_16x16x32_bf16 v[104:107], v[144:147], v[184:187], v[104:107]
	v_mfma_f32_16x16x32_bf16 v[92:95], v[136:139], v[192:195], v[92:95]
	v_mfma_f32_16x16x32_bf16 v[88:91], v[144:147], v[192:195], v[88:91]
	v_mfma_f32_16x16x32_bf16 v[132:135], v[140:143], v[172:175], v[132:135]
	v_mfma_f32_16x16x32_bf16 v[128:131], v[148:151], v[172:175], v[128:131]
	v_mfma_f32_16x16x32_bf16 v[124:127], v[140:143], v[180:183], v[124:127]
	v_mfma_f32_16x16x32_bf16 v[120:123], v[148:151], v[180:183], v[120:123]
	v_mfma_f32_16x16x32_bf16 v[108:111], v[140:143], v[188:191], v[108:111]
	v_mfma_f32_16x16x32_bf16 v[104:107], v[148:151], v[188:191], v[104:107]
	v_mfma_f32_16x16x32_bf16 v[92:95], v[140:143], v[196:199], v[92:95]
	v_mfma_f32_16x16x32_bf16 v[88:91], v[148:151], v[196:199], v[88:91]
	s_setprio 0
	s_setprio 1
	v_mfma_f32_16x16x32_bf16 v[116:119], v[152:155], v[168:171], v[116:119]
	v_mfma_f32_16x16x32_bf16 v[112:115], v[160:163], v[168:171], v[112:115]
	v_mfma_f32_16x16x32_bf16 v[100:103], v[152:155], v[176:179], v[100:103]
	v_mfma_f32_16x16x32_bf16 v[96:99], v[160:163], v[176:179], v[96:99]
	v_mfma_f32_16x16x32_bf16 v[80:83], v[152:155], v[184:187], v[80:83]
	v_mfma_f32_16x16x32_bf16 v[76:79], v[160:163], v[184:187], v[76:79]
	v_mfma_f32_16x16x32_bf16 v[72:75], v[152:155], v[192:195], v[72:75]
	v_mfma_f32_16x16x32_bf16 v[68:71], v[160:163], v[192:195], v[68:71]
	v_mfma_f32_16x16x32_bf16 v[116:119], v[156:159], v[172:175], v[116:119]
	v_mfma_f32_16x16x32_bf16 v[112:115], v[164:167], v[172:175], v[112:115]
	v_mfma_f32_16x16x32_bf16 v[100:103], v[156:159], v[180:183], v[100:103]
	v_mfma_f32_16x16x32_bf16 v[96:99], v[164:167], v[180:183], v[96:99]
	v_mfma_f32_16x16x32_bf16 v[80:83], v[156:159], v[188:191], v[80:83]
	v_mfma_f32_16x16x32_bf16 v[76:79], v[164:167], v[188:191], v[76:79]
	v_mfma_f32_16x16x32_bf16 v[72:75], v[156:159], v[196:199], v[72:75]
	v_mfma_f32_16x16x32_bf16 v[68:71], v[164:167], v[196:199], v[68:71]
	s_setprio 0
	s_barrier
	s_add_i32 s42, s62, s44
	v_lshl_add_u64 v[224:225], s[40:41], 0, v[210:211]
	s_mov_b32 m0, s42
	ds_read_b128 v[168:171], v244 offset:49152
	ds_read_b128 v[172:175], v244 offset:50176
	ds_read_b128 v[176:179], v244 offset:51200
	ds_read_b128 v[180:183], v244 offset:52224
	ds_read_b128 v[184:187], v244 offset:53248
	ds_read_b128 v[188:191], v244 offset:54272
	ds_read_b128 v[192:195], v244 offset:55296
	ds_read_b128 v[196:199], v244 offset:56320
	global_load_lds_dwordx4 v[224:225], off
	s_add_i32 m0, s42, 0x2000
	s_add_u32 s38, s38, 0xc000
	v_lshl_add_u64 v[224:225], s[40:41], 0, v[208:209]
	s_addc_u32 s39, s39, 0
	s_add_i32 s40, s63, s44
	global_load_lds_dwordx4 v[224:225], off
	v_lshl_add_u64 v[224:225], s[38:39], 0, v[210:211]
	s_mov_b32 m0, s40
	v_lshl_add_u64 v[204:205], v[204:205], 0, s[36:37]
	global_load_lds_dwordx4 v[224:225], off
	v_lshl_add_u64 v[224:225], s[38:39], 0, v[208:209]
	s_add_i32 m0, s40, 0x2000
	s_nop 0
	global_load_lds_dwordx4 v[224:225], off
	s_mov_b32 m0, s54
	s_nop 0
	global_load_lds_dwordx4 v[204:205], off
	v_lshl_add_u64 v[204:205], v[248:249], 0, s[36:37]
	s_mov_b32 m0, s55
	s_nop 0
	global_load_lds_dwordx4 v[204:205], off
	s_waitcnt vmcnt(8)
	s_waitcnt lgkmcnt(0)
	s_barrier
	s_setprio 1
	s_waitcnt lgkmcnt(0)
	v_mfma_f32_16x16x32_bf16 v[64:67], v[136:139], v[168:171], v[64:67]
	v_mfma_f32_16x16x32_bf16 v[60:63], v[144:147], v[168:171], v[60:63]
	v_mfma_f32_16x16x32_bf16 v[56:59], v[136:139], v[176:179], v[56:59]
	v_mfma_f32_16x16x32_bf16 v[52:55], v[144:147], v[176:179], v[52:55]
	v_mfma_f32_16x16x32_bf16 v[40:43], v[136:139], v[184:187], v[40:43]
	v_mfma_f32_16x16x32_bf16 v[36:39], v[144:147], v[184:187], v[36:39]
	v_mfma_f32_16x16x32_bf16 v[24:27], v[136:139], v[192:195], v[24:27]
	v_mfma_f32_16x16x32_bf16 v[20:23], v[144:147], v[192:195], v[20:23]
	v_mfma_f32_16x16x32_bf16 v[64:67], v[140:143], v[172:175], v[64:67]
	v_mfma_f32_16x16x32_bf16 v[60:63], v[148:151], v[172:175], v[60:63]
	v_mfma_f32_16x16x32_bf16 v[56:59], v[140:143], v[180:183], v[56:59]
	v_mfma_f32_16x16x32_bf16 v[52:55], v[148:151], v[180:183], v[52:55]
	v_mfma_f32_16x16x32_bf16 v[40:43], v[140:143], v[188:191], v[40:43]
	v_mfma_f32_16x16x32_bf16 v[36:39], v[148:151], v[188:191], v[36:39]
	v_mfma_f32_16x16x32_bf16 v[24:27], v[140:143], v[196:199], v[24:27]
	v_mfma_f32_16x16x32_bf16 v[20:23], v[148:151], v[196:199], v[20:23]
	s_setprio 0
	s_setprio 1
	v_mfma_f32_16x16x32_bf16 v[48:51], v[152:155], v[168:171], v[48:51]
	v_mfma_f32_16x16x32_bf16 v[44:47], v[160:163], v[168:171], v[44:47]
	v_mfma_f32_16x16x32_bf16 v[32:35], v[152:155], v[176:179], v[32:35]
	v_mfma_f32_16x16x32_bf16 v[28:31], v[160:163], v[176:179], v[28:31]
	v_mfma_f32_16x16x32_bf16 v[16:19], v[152:155], v[184:187], v[16:19]
	v_mfma_f32_16x16x32_bf16 v[12:15], v[160:163], v[184:187], v[12:15]
	v_mfma_f32_16x16x32_bf16 v[8:11], v[152:155], v[192:195], v[8:11]
	v_mfma_f32_16x16x32_bf16 v[4:7], v[160:163], v[192:195], v[4:7]
	v_mfma_f32_16x16x32_bf16 v[48:51], v[156:159], v[172:175], v[48:51]
	v_mfma_f32_16x16x32_bf16 v[44:47], v[164:167], v[172:175], v[44:47]
	v_mfma_f32_16x16x32_bf16 v[32:35], v[156:159], v[180:183], v[32:35]
	v_mfma_f32_16x16x32_bf16 v[28:31], v[164:167], v[180:183], v[28:31]
	v_mfma_f32_16x16x32_bf16 v[16:19], v[156:159], v[188:191], v[16:19]
	v_mfma_f32_16x16x32_bf16 v[12:15], v[164:167], v[188:191], v[12:15]
	v_mfma_f32_16x16x32_bf16 v[8:11], v[156:159], v[196:199], v[8:11]
	v_mfma_f32_16x16x32_bf16 v[4:7], v[164:167], v[196:199], v[4:7]
	s_setprio 0
	s_barrier
	s_add_i32 s61, s61, 2
	s_add_u32 s59, s59, 0x10000
	s_addc_u32 s60, s60, 0
	s_add_u32 s14, s14, 0x100
	s_addc_u32 s15, s15, 0
	s_cmp_gt_u32 s61, 29
	s_cbranch_scc1 .LBB0_297

.LBB0_498:
	s_add_u32 s38, s12, 0x80
	s_addc_u32 s39, s13, 0
	s_waitcnt vmcnt(8)
	s_and_b64 s[14:15], s[14:15], exec
	s_waitcnt lgkmcnt(0)
	s_cselect_b32 s14, s60, s61
	s_cselect_b32 s41, s31, s39
	s_cselect_b32 s40, s30, s38
	s_cselect_b32 s15, s9, s62
	s_add_u32 s38, s14, 0x8000
	s_addc_u32 s39, s15, 0
	s_barrier
	s_setprio 1
	s_waitcnt lgkmcnt(0)
	v_mfma_f32_16x16x32_bf16 v[132:135], v[152:155], v[192:195], v[132:135]
	v_mfma_f32_16x16x32_bf16 v[128:131], v[160:163], v[192:195], v[128:131]
	v_mfma_f32_16x16x32_bf16 v[124:127], v[152:155], v[184:187], v[124:127]
	v_mfma_f32_16x16x32_bf16 v[120:123], v[160:163], v[184:187], v[120:123]
	v_mfma_f32_16x16x32_bf16 v[108:111], v[152:155], v[176:179], v[108:111]
	v_mfma_f32_16x16x32_bf16 v[104:107], v[160:163], v[176:179], v[104:107]
	v_mfma_f32_16x16x32_bf16 v[92:95], v[152:155], v[168:171], v[92:95]
	v_mfma_f32_16x16x32_bf16 v[88:91], v[160:163], v[168:171], v[88:91]
	v_mfma_f32_16x16x32_bf16 v[132:135], v[156:159], v[196:199], v[132:135]
	v_mfma_f32_16x16x32_bf16 v[128:131], v[164:167], v[196:199], v[128:131]
	v_mfma_f32_16x16x32_bf16 v[124:127], v[156:159], v[188:191], v[124:127]
	v_mfma_f32_16x16x32_bf16 v[120:123], v[164:167], v[188:191], v[120:123]
	v_mfma_f32_16x16x32_bf16 v[108:111], v[156:159], v[180:183], v[108:111]
	v_mfma_f32_16x16x32_bf16 v[104:107], v[164:167], v[180:183], v[104:107]
	v_mfma_f32_16x16x32_bf16 v[92:95], v[156:159], v[172:175], v[92:95]
	v_mfma_f32_16x16x32_bf16 v[88:91], v[164:167], v[172:175], v[88:91]
	s_setprio 0
	s_setprio 1
	v_mfma_f32_16x16x32_bf16 v[116:119], v[136:139], v[192:195], v[116:119]
	v_mfma_f32_16x16x32_bf16 v[112:115], v[144:147], v[192:195], v[112:115]
	v_mfma_f32_16x16x32_bf16 v[100:103], v[136:139], v[184:187], v[100:103]
	v_mfma_f32_16x16x32_bf16 v[96:99], v[144:147], v[184:187], v[96:99]
	v_mfma_f32_16x16x32_bf16 v[80:83], v[136:139], v[176:179], v[80:83]
	v_mfma_f32_16x16x32_bf16 v[76:79], v[144:147], v[176:179], v[76:79]
	v_mfma_f32_16x16x32_bf16 v[72:75], v[136:139], v[168:171], v[72:75]
	v_mfma_f32_16x16x32_bf16 v[68:71], v[144:147], v[168:171], v[68:71]
	v_mfma_f32_16x16x32_bf16 v[116:119], v[140:143], v[196:199], v[116:119]
	v_mfma_f32_16x16x32_bf16 v[112:115], v[148:151], v[196:199], v[112:115]
	v_mfma_f32_16x16x32_bf16 v[100:103], v[140:143], v[188:191], v[100:103]
	v_mfma_f32_16x16x32_bf16 v[96:99], v[148:151], v[188:191], v[96:99]
	v_mfma_f32_16x16x32_bf16 v[80:83], v[140:143], v[180:183], v[80:83]
	v_mfma_f32_16x16x32_bf16 v[76:79], v[148:151], v[180:183], v[76:79]
	v_mfma_f32_16x16x32_bf16 v[72:75], v[140:143], v[172:175], v[72:75]
	v_mfma_f32_16x16x32_bf16 v[68:71], v[148:151], v[172:175], v[68:71]
	s_setprio 0
	s_barrier
	s_mov_b32 m0, s44
	v_lshl_add_u64 v[246:247], s[14:15], 0, v[210:211]
	s_add_u32 s64, s14, 0x4000
	ds_read_b128 v[168:171], v243 offset:16384
	ds_read_b128 v[172:175], v243 offset:17408
	ds_read_b128 v[176:179], v243 offset:18432
	ds_read_b128 v[180:183], v243 offset:19456
	ds_read_b128 v[184:187], v243 offset:20480
	ds_read_b128 v[188:191], v243 offset:21504
	ds_read_b128 v[192:195], v243 offset:22528
	ds_read_b128 v[196:199], v243 offset:23552
	global_load_lds_dwordx4 v[246:247], off
	v_lshl_add_u64 v[246:247], s[14:15], 0, v[208:209]
	s_mov_b32 m0, s45
	s_addc_u32 s65, s15, 0
	global_load_lds_dwordx4 v[246:247], off
	v_lshl_add_u64 v[246:247], s[64:65], 0, v[210:211]
	s_mov_b32 m0, s47
	v_mov_b32_e32 v215, v3
	global_load_lds_dwordx4 v[246:247], off
	v_lshl_add_u64 v[246:247], s[64:65], 0, v[208:209]
	s_mov_b32 m0, s48
	v_lshl_add_u64 v[248:249], s[40:41], 0, v[214:215]
	global_load_lds_dwordx4 v[246:247], off
	s_mov_b32 m0, s43
	v_lshl_add_u64 v[246:247], s[40:41], 0, v[2:3]
	global_load_lds_dwordx4 v2, s[40:41]
	s_waitcnt vmcnt(7)
	s_waitcnt lgkmcnt(0)
	s_barrier
	s_setprio 1
	s_waitcnt lgkmcnt(0)
	v_mfma_f32_16x16x32_bf16 v[64:67], v[152:155], v[168:171], v[64:67]
	v_mfma_f32_16x16x32_bf16 v[60:63], v[160:163], v[168:171], v[60:63]
	v_mfma_f32_16x16x32_bf16 v[56:59], v[152:155], v[176:179], v[56:59]
	v_mfma_f32_16x16x32_bf16 v[52:55], v[160:163], v[176:179], v[52:55]
	v_mfma_f32_16x16x32_bf16 v[40:43], v[152:155], v[184:187], v[40:43]
	v_mfma_f32_16x16x32_bf16 v[36:39], v[160:163], v[184:187], v[36:39]
	v_mfma_f32_16x16x32_bf16 v[24:27], v[152:155], v[192:195], v[24:27]
	v_mfma_f32_16x16x32_bf16 v[20:23], v[160:163], v[192:195], v[20:23]
	v_mfma_f32_16x16x32_bf16 v[64:67], v[156:159], v[172:175], v[64:67]
	v_mfma_f32_16x16x32_bf16 v[60:63], v[164:167], v[172:175], v[60:63]
	v_mfma_f32_16x16x32_bf16 v[56:59], v[156:159], v[180:183], v[56:59]
	v_mfma_f32_16x16x32_bf16 v[52:55], v[164:167], v[180:183], v[52:55]
	v_mfma_f32_16x16x32_bf16 v[40:43], v[156:159], v[188:191], v[40:43]
	v_mfma_f32_16x16x32_bf16 v[36:39], v[164:167], v[188:191], v[36:39]
	v_mfma_f32_16x16x32_bf16 v[24:27], v[156:159], v[196:199], v[24:27]
	v_mfma_f32_16x16x32_bf16 v[20:23], v[164:167], v[196:199], v[20:23]
	s_setprio 0
	s_setprio 1
	v_mfma_f32_16x16x32_bf16 v[48:51], v[136:139], v[168:171], v[48:51]
	v_mfma_f32_16x16x32_bf16 v[44:47], v[144:147], v[168:171], v[44:47]
	v_mfma_f32_16x16x32_bf16 v[32:35], v[136:139], v[176:179], v[32:35]
	v_mfma_f32_16x16x32_bf16 v[28:31], v[144:147], v[176:179], v[28:31]
	v_mfma_f32_16x16x32_bf16 v[16:19], v[136:139], v[184:187], v[16:19]
	v_mfma_f32_16x16x32_bf16 v[12:15], v[144:147], v[184:187], v[12:15]
	v_mfma_f32_16x16x32_bf16 v[8:11], v[136:139], v[192:195], v[8:11]
	v_mfma_f32_16x16x32_bf16 v[4:7], v[144:147], v[192:195], v[4:7]
	v_mfma_f32_16x16x32_bf16 v[48:51], v[140:143], v[172:175], v[48:51]
	v_mfma_f32_16x16x32_bf16 v[44:47], v[148:151], v[172:175], v[44:47]
	v_mfma_f32_16x16x32_bf16 v[32:35], v[140:143], v[180:183], v[32:35]
	v_mfma_f32_16x16x32_bf16 v[28:31], v[148:151], v[180:183], v[28:31]
	v_mfma_f32_16x16x32_bf16 v[16:19], v[140:143], v[188:191], v[16:19]
	v_mfma_f32_16x16x32_bf16 v[12:15], v[148:151], v[188:191], v[12:15]
	v_mfma_f32_16x16x32_bf16 v[8:11], v[140:143], v[196:199], v[8:11]
	v_mfma_f32_16x16x32_bf16 v[4:7], v[148:151], v[196:199], v[4:7]
	s_setprio 0
	s_barrier
	s_mov_b32 m0, s49
	s_nop 0
	global_load_lds_dwordx4 v214, s[40:41]
	s_add_i32 s64, 0, 0x18000
	s_add_i32 s65, 0, 0x1c000
	v_add_u32_e32 v148, s64, v241
	v_add_u32_e32 v164, s65, v241
	ds_read_b128 v[136:139], v148
	ds_read_b128 v[140:143], v148 offset:1024
	ds_read_b128 v[144:147], v148 offset:2048
	ds_read_b128 v[148:151], v148 offset:3072
	ds_read_b128 v[152:155], v164
	ds_read_b128 v[156:159], v164 offset:1024
	ds_read_b128 v[160:163], v164 offset:2048
	ds_read_b128 v[164:167], v164 offset:3072
	s_mov_b32 m0, s50
	v_lshl_add_u64 v[224:225], s[40:41], 0, v[224:225]
	ds_read_b128 v[168:171], v243 offset:32768
	ds_read_b128 v[172:175], v243 offset:33792
	ds_read_b128 v[176:179], v243 offset:34816
	ds_read_b128 v[180:183], v243 offset:35840
	ds_read_b128 v[184:187], v243 offset:36864
	ds_read_b128 v[188:191], v243 offset:37888
	ds_read_b128 v[192:195], v243 offset:38912
	ds_read_b128 v[196:199], v243 offset:39936
	global_load_lds_dwordx4 v[224:225], off
	v_lshl_add_u64 v[222:223], s[40:41], 0, v[222:223]
	s_mov_b32 m0, s51
	s_nop 0
	global_load_lds_dwordx4 v[222:223], off
	s_waitcnt vmcnt(8)
	s_waitcnt lgkmcnt(0)
	s_barrier
	s_setprio 1
	s_waitcnt lgkmcnt(0)
	v_mfma_f32_16x16x32_bf16 v[132:135], v[136:139], v[168:171], v[132:135]
	v_mfma_f32_16x16x32_bf16 v[128:131], v[144:147], v[168:171], v[128:131]
	v_mfma_f32_16x16x32_bf16 v[124:127], v[136:139], v[176:179], v[124:127]
	v_mfma_f32_16x16x32_bf16 v[120:123], v[144:147], v[176:179], v[120:123]
	v_mfma_f32_16x16x32_bf16 v[108:111], v[136:139], v[184:187], v[108:111]
	v_mfma_f32_16x16x32_bf16 v[104:107], v[144:147], v[184:187], v[104:107]
	v_mfma_f32_16x16x32_bf16 v[92:95], v[136:139], v[192:195], v[92:95]
	v_mfma_f32_16x16x32_bf16 v[88:91], v[144:147], v[192:195], v[88:91]
	v_mfma_f32_16x16x32_bf16 v[132:135], v[140:143], v[172:175], v[132:135]
	v_mfma_f32_16x16x32_bf16 v[128:131], v[148:151], v[172:175], v[128:131]
	v_mfma_f32_16x16x32_bf16 v[124:127], v[140:143], v[180:183], v[124:127]
	v_mfma_f32_16x16x32_bf16 v[120:123], v[148:151], v[180:183], v[120:123]
	v_mfma_f32_16x16x32_bf16 v[108:111], v[140:143], v[188:191], v[108:111]
	v_mfma_f32_16x16x32_bf16 v[104:107], v[148:151], v[188:191], v[104:107]
	v_mfma_f32_16x16x32_bf16 v[92:95], v[140:143], v[196:199], v[92:95]
	v_mfma_f32_16x16x32_bf16 v[88:91], v[148:151], v[196:199], v[88:91]
	s_setprio 0
	s_setprio 1
	v_mfma_f32_16x16x32_bf16 v[116:119], v[152:155], v[168:171], v[116:119]
	v_mfma_f32_16x16x32_bf16 v[112:115], v[160:163], v[168:171], v[112:115]
	v_mfma_f32_16x16x32_bf16 v[100:103], v[152:155], v[176:179], v[100:103]
	v_mfma_f32_16x16x32_bf16 v[96:99], v[160:163], v[176:179], v[96:99]
	v_mfma_f32_16x16x32_bf16 v[80:83], v[152:155], v[184:187], v[80:83]
	v_mfma_f32_16x16x32_bf16 v[76:79], v[160:163], v[184:187], v[76:79]
	v_mfma_f32_16x16x32_bf16 v[72:75], v[152:155], v[192:195], v[72:75]
	v_mfma_f32_16x16x32_bf16 v[68:71], v[160:163], v[192:195], v[68:71]
	v_mfma_f32_16x16x32_bf16 v[116:119], v[156:159], v[172:175], v[116:119]
	v_mfma_f32_16x16x32_bf16 v[112:115], v[164:167], v[172:175], v[112:115]
	v_mfma_f32_16x16x32_bf16 v[100:103], v[156:159], v[180:183], v[100:103]
	v_mfma_f32_16x16x32_bf16 v[96:99], v[164:167], v[180:183], v[96:99]
	v_mfma_f32_16x16x32_bf16 v[80:83], v[156:159], v[188:191], v[80:83]
	v_mfma_f32_16x16x32_bf16 v[76:79], v[164:167], v[188:191], v[76:79]
	v_mfma_f32_16x16x32_bf16 v[72:75], v[156:159], v[196:199], v[72:75]
	v_mfma_f32_16x16x32_bf16 v[68:71], v[164:167], v[196:199], v[68:71]
	s_setprio 0
	s_barrier
	s_add_i32 s40, s64, s42
	v_lshl_add_u64 v[222:223], s[38:39], 0, v[210:211]
	s_mov_b32 m0, s40
	ds_read_b128 v[168:171], v243 offset:49152
	ds_read_b128 v[172:175], v243 offset:50176
	ds_read_b128 v[176:179], v243 offset:51200
	ds_read_b128 v[180:183], v243 offset:52224
	ds_read_b128 v[184:187], v243 offset:53248
	ds_read_b128 v[188:191], v243 offset:54272
	ds_read_b128 v[192:195], v243 offset:55296
	ds_read_b128 v[196:199], v243 offset:56320
	global_load_lds_dwordx4 v[222:223], off
	s_add_i32 m0, s40, 0x2000
	s_add_u32 s14, s14, 0xc000
	v_lshl_add_u64 v[222:223], s[38:39], 0, v[208:209]
	s_addc_u32 s15, s15, 0
	s_add_i32 s38, s65, s42
	global_load_lds_dwordx4 v[222:223], off
	v_lshl_add_u64 v[222:223], s[14:15], 0, v[210:211]
	s_mov_b32 m0, s38
	s_nop 0
	global_load_lds_dwordx4 v[222:223], off
	v_lshl_add_u64 v[222:223], s[14:15], 0, v[208:209]
	s_add_i32 m0, s38, 0x2000
	s_nop 0
	global_load_lds_dwordx4 v[222:223], off
	v_lshl_add_u64 v[222:223], v[246:247], 0, s[36:37]
	s_mov_b32 m0, s53
	s_nop 0
	global_load_lds_dwordx4 v[222:223], off
	v_lshl_add_u64 v[222:223], v[248:249], 0, s[36:37]
	s_mov_b32 m0, s54
	s_nop 0
	global_load_lds_dwordx4 v[222:223], off
	s_waitcnt vmcnt(8)
	s_waitcnt lgkmcnt(0)
	s_barrier
	s_setprio 1
	s_waitcnt lgkmcnt(0)
	v_mfma_f32_16x16x32_bf16 v[64:67], v[136:139], v[168:171], v[64:67]
	v_mfma_f32_16x16x32_bf16 v[60:63], v[144:147], v[168:171], v[60:63]
	v_mfma_f32_16x16x32_bf16 v[56:59], v[136:139], v[176:179], v[56:59]
	v_mfma_f32_16x16x32_bf16 v[52:55], v[144:147], v[176:179], v[52:55]
	v_mfma_f32_16x16x32_bf16 v[40:43], v[136:139], v[184:187], v[40:43]
	v_mfma_f32_16x16x32_bf16 v[36:39], v[144:147], v[184:187], v[36:39]
	v_mfma_f32_16x16x32_bf16 v[24:27], v[136:139], v[192:195], v[24:27]
	v_mfma_f32_16x16x32_bf16 v[20:23], v[144:147], v[192:195], v[20:23]
	v_mfma_f32_16x16x32_bf16 v[64:67], v[140:143], v[172:175], v[64:67]
	v_mfma_f32_16x16x32_bf16 v[60:63], v[148:151], v[172:175], v[60:63]
	v_mfma_f32_16x16x32_bf16 v[56:59], v[140:143], v[180:183], v[56:59]
	v_mfma_f32_16x16x32_bf16 v[52:55], v[148:151], v[180:183], v[52:55]
	v_mfma_f32_16x16x32_bf16 v[40:43], v[140:143], v[188:191], v[40:43]
	v_mfma_f32_16x16x32_bf16 v[36:39], v[148:151], v[188:191], v[36:39]
	v_mfma_f32_16x16x32_bf16 v[24:27], v[140:143], v[196:199], v[24:27]
	v_mfma_f32_16x16x32_bf16 v[20:23], v[148:151], v[196:199], v[20:23]
	s_setprio 0
	s_setprio 1
	v_mfma_f32_16x16x32_bf16 v[48:51], v[152:155], v[168:171], v[48:51]
	v_mfma_f32_16x16x32_bf16 v[44:47], v[160:163], v[168:171], v[44:47]
	v_mfma_f32_16x16x32_bf16 v[32:35], v[152:155], v[176:179], v[32:35]
	v_mfma_f32_16x16x32_bf16 v[28:31], v[160:163], v[176:179], v[28:31]
	v_mfma_f32_16x16x32_bf16 v[16:19], v[152:155], v[184:187], v[16:19]
	v_mfma_f32_16x16x32_bf16 v[12:15], v[160:163], v[184:187], v[12:15]
	v_mfma_f32_16x16x32_bf16 v[8:11], v[152:155], v[192:195], v[8:11]
	v_mfma_f32_16x16x32_bf16 v[4:7], v[160:163], v[192:195], v[4:7]
	v_mfma_f32_16x16x32_bf16 v[48:51], v[156:159], v[172:175], v[48:51]
	v_mfma_f32_16x16x32_bf16 v[44:47], v[164:167], v[172:175], v[44:47]
	v_mfma_f32_16x16x32_bf16 v[32:35], v[156:159], v[180:183], v[32:35]
	v_mfma_f32_16x16x32_bf16 v[28:31], v[164:167], v[180:183], v[28:31]
	v_mfma_f32_16x16x32_bf16 v[16:19], v[156:159], v[188:191], v[16:19]
	v_mfma_f32_16x16x32_bf16 v[12:15], v[164:167], v[188:191], v[12:15]
	v_mfma_f32_16x16x32_bf16 v[8:11], v[156:159], v[196:199], v[8:11]
	v_mfma_f32_16x16x32_bf16 v[4:7], v[164:167], v[196:199], v[4:7]
	s_setprio 0
	s_barrier
	s_add_i32 s63, s63, 2
	s_add_u32 s61, s61, 0x10000
	s_addc_u32 s62, s62, 0
	s_add_u32 s12, s12, 0x100
	s_addc_u32 s13, s13, 0
	s_cmp_gt_u32 s63, 29
	s_cbranch_scc1 .LBB0_501

.LBB0_835:
	s_add_u32 s40, s14, 0x80
	s_addc_u32 s41, s15, 0
	s_waitcnt vmcnt(8)
	s_and_b64 s[38:39], s[38:39], exec
	s_waitcnt lgkmcnt(0)
	s_cselect_b32 s38, s13, s59
	s_cselect_b32 s43, s1, s41
	s_cselect_b32 s42, s0, s40
	s_cselect_b32 s39, s9, s60
	s_add_u32 s40, s38, 0x8000
	s_addc_u32 s41, s39, 0
	s_barrier
	s_setprio 1
	s_waitcnt lgkmcnt(0)
	v_mfma_f32_16x16x32_bf16 v[132:135], v[152:155], v[192:195], v[132:135]
	v_mfma_f32_16x16x32_bf16 v[128:131], v[160:163], v[192:195], v[128:131]
	v_mfma_f32_16x16x32_bf16 v[124:127], v[152:155], v[184:187], v[124:127]
	v_mfma_f32_16x16x32_bf16 v[120:123], v[160:163], v[184:187], v[120:123]
	v_mfma_f32_16x16x32_bf16 v[108:111], v[152:155], v[176:179], v[108:111]
	v_mfma_f32_16x16x32_bf16 v[104:107], v[160:163], v[176:179], v[104:107]
	v_mfma_f32_16x16x32_bf16 v[92:95], v[152:155], v[168:171], v[92:95]
	v_mfma_f32_16x16x32_bf16 v[88:91], v[160:163], v[168:171], v[88:91]
	v_mfma_f32_16x16x32_bf16 v[132:135], v[156:159], v[196:199], v[132:135]
	v_mfma_f32_16x16x32_bf16 v[128:131], v[164:167], v[196:199], v[128:131]
	v_mfma_f32_16x16x32_bf16 v[124:127], v[156:159], v[188:191], v[124:127]
	v_mfma_f32_16x16x32_bf16 v[120:123], v[164:167], v[188:191], v[120:123]
	v_mfma_f32_16x16x32_bf16 v[108:111], v[156:159], v[180:183], v[108:111]
	v_mfma_f32_16x16x32_bf16 v[104:107], v[164:167], v[180:183], v[104:107]
	v_mfma_f32_16x16x32_bf16 v[92:95], v[156:159], v[172:175], v[92:95]
	v_mfma_f32_16x16x32_bf16 v[88:91], v[164:167], v[172:175], v[88:91]
	s_setprio 0
	s_setprio 1
	v_mfma_f32_16x16x32_bf16 v[116:119], v[136:139], v[192:195], v[116:119]
	v_mfma_f32_16x16x32_bf16 v[112:115], v[144:147], v[192:195], v[112:115]
	v_mfma_f32_16x16x32_bf16 v[100:103], v[136:139], v[184:187], v[100:103]
	v_mfma_f32_16x16x32_bf16 v[96:99], v[144:147], v[184:187], v[96:99]
	v_mfma_f32_16x16x32_bf16 v[80:83], v[136:139], v[176:179], v[80:83]
	v_mfma_f32_16x16x32_bf16 v[76:79], v[144:147], v[176:179], v[76:79]
	v_mfma_f32_16x16x32_bf16 v[72:75], v[136:139], v[168:171], v[72:75]
	v_mfma_f32_16x16x32_bf16 v[68:71], v[144:147], v[168:171], v[68:71]
	v_mfma_f32_16x16x32_bf16 v[116:119], v[140:143], v[196:199], v[116:119]
	v_mfma_f32_16x16x32_bf16 v[112:115], v[148:151], v[196:199], v[112:115]
	v_mfma_f32_16x16x32_bf16 v[100:103], v[140:143], v[188:191], v[100:103]
	v_mfma_f32_16x16x32_bf16 v[96:99], v[148:151], v[188:191], v[96:99]
	v_mfma_f32_16x16x32_bf16 v[80:83], v[140:143], v[180:183], v[80:83]
	v_mfma_f32_16x16x32_bf16 v[76:79], v[148:151], v[180:183], v[76:79]
	v_mfma_f32_16x16x32_bf16 v[72:75], v[140:143], v[172:175], v[72:75]
	v_mfma_f32_16x16x32_bf16 v[68:71], v[148:151], v[172:175], v[68:71]
	s_setprio 0
	s_barrier
	s_mov_b32 m0, s47
	v_lshl_add_u64 v[248:249], s[38:39], 0, v[210:211]
	s_add_u32 s62, s38, 0x4000
	ds_read_b128 v[168:171], v244 offset:16384
	ds_read_b128 v[172:175], v244 offset:17408
	ds_read_b128 v[176:179], v244 offset:18432
	ds_read_b128 v[180:183], v244 offset:19456
	ds_read_b128 v[184:187], v244 offset:20480
	ds_read_b128 v[188:191], v244 offset:21504
	ds_read_b128 v[192:195], v244 offset:22528
	ds_read_b128 v[196:199], v244 offset:23552
	global_load_lds_dwordx4 v[248:249], off
	v_lshl_add_u64 v[248:249], s[38:39], 0, v[208:209]
	s_mov_b32 m0, s48
	s_addc_u32 s63, s39, 0
	global_load_lds_dwordx4 v[248:249], off
	v_lshl_add_u64 v[248:249], s[62:63], 0, v[210:211]
	s_mov_b32 m0, s49
	v_mov_b32_e32 v215, v3
	global_load_lds_dwordx4 v[248:249], off
	v_lshl_add_u64 v[248:249], s[62:63], 0, v[208:209]
	s_mov_b32 m0, s50
	v_lshl_add_u64 v[204:205], s[42:43], 0, v[214:215]
	global_load_lds_dwordx4 v[248:249], off
	s_mov_b32 m0, s45
	v_lshl_add_u64 v[248:249], s[42:43], 0, v[2:3]
	global_load_lds_dwordx4 v2, s[42:43]
	s_waitcnt vmcnt(7)
	s_waitcnt lgkmcnt(0)
	s_barrier
	s_setprio 1
	s_waitcnt lgkmcnt(0)
	v_mfma_f32_16x16x32_bf16 v[64:67], v[152:155], v[168:171], v[64:67]
	v_mfma_f32_16x16x32_bf16 v[60:63], v[160:163], v[168:171], v[60:63]
	v_mfma_f32_16x16x32_bf16 v[56:59], v[152:155], v[176:179], v[56:59]
	v_mfma_f32_16x16x32_bf16 v[52:55], v[160:163], v[176:179], v[52:55]
	v_mfma_f32_16x16x32_bf16 v[40:43], v[152:155], v[184:187], v[40:43]
	v_mfma_f32_16x16x32_bf16 v[36:39], v[160:163], v[184:187], v[36:39]
	v_mfma_f32_16x16x32_bf16 v[24:27], v[152:155], v[192:195], v[24:27]
	v_mfma_f32_16x16x32_bf16 v[20:23], v[160:163], v[192:195], v[20:23]
	v_mfma_f32_16x16x32_bf16 v[64:67], v[156:159], v[172:175], v[64:67]
	v_mfma_f32_16x16x32_bf16 v[60:63], v[164:167], v[172:175], v[60:63]
	v_mfma_f32_16x16x32_bf16 v[56:59], v[156:159], v[180:183], v[56:59]
	v_mfma_f32_16x16x32_bf16 v[52:55], v[164:167], v[180:183], v[52:55]
	v_mfma_f32_16x16x32_bf16 v[40:43], v[156:159], v[188:191], v[40:43]
	v_mfma_f32_16x16x32_bf16 v[36:39], v[164:167], v[188:191], v[36:39]
	v_mfma_f32_16x16x32_bf16 v[24:27], v[156:159], v[196:199], v[24:27]
	v_mfma_f32_16x16x32_bf16 v[20:23], v[164:167], v[196:199], v[20:23]
	s_setprio 0
	s_setprio 1
	v_mfma_f32_16x16x32_bf16 v[48:51], v[136:139], v[168:171], v[48:51]
	v_mfma_f32_16x16x32_bf16 v[44:47], v[144:147], v[168:171], v[44:47]
	v_mfma_f32_16x16x32_bf16 v[32:35], v[136:139], v[176:179], v[32:35]
	v_mfma_f32_16x16x32_bf16 v[28:31], v[144:147], v[176:179], v[28:31]
	v_mfma_f32_16x16x32_bf16 v[16:19], v[136:139], v[184:187], v[16:19]
	v_mfma_f32_16x16x32_bf16 v[12:15], v[144:147], v[184:187], v[12:15]
	v_mfma_f32_16x16x32_bf16 v[8:11], v[136:139], v[192:195], v[8:11]
	v_mfma_f32_16x16x32_bf16 v[4:7], v[144:147], v[192:195], v[4:7]
	v_mfma_f32_16x16x32_bf16 v[48:51], v[140:143], v[172:175], v[48:51]
	v_mfma_f32_16x16x32_bf16 v[44:47], v[148:151], v[172:175], v[44:47]
	v_mfma_f32_16x16x32_bf16 v[32:35], v[140:143], v[180:183], v[32:35]
	v_mfma_f32_16x16x32_bf16 v[28:31], v[148:151], v[180:183], v[28:31]
	v_mfma_f32_16x16x32_bf16 v[16:19], v[140:143], v[188:191], v[16:19]
	v_mfma_f32_16x16x32_bf16 v[12:15], v[148:151], v[188:191], v[12:15]
	v_mfma_f32_16x16x32_bf16 v[8:11], v[140:143], v[196:199], v[8:11]
	v_mfma_f32_16x16x32_bf16 v[4:7], v[148:151], v[196:199], v[4:7]
	s_setprio 0
	s_barrier
	s_mov_b32 m0, s51
	s_nop 0
	global_load_lds_dwordx4 v214, s[42:43]
	s_add_i32 s62, 0, 0x18000
	s_add_i32 s63, 0, 0x1c000
	v_add_u32_e32 v148, s62, v243
	v_add_u32_e32 v164, s63, v243
	ds_read_b128 v[136:139], v148
	ds_read_b128 v[140:143], v148 offset:1024
	ds_read_b128 v[144:147], v148 offset:2048
	ds_read_b128 v[148:151], v148 offset:3072
	ds_read_b128 v[152:155], v164
	ds_read_b128 v[156:159], v164 offset:1024
	ds_read_b128 v[160:163], v164 offset:2048
	ds_read_b128 v[164:167], v164 offset:3072
	s_mov_b32 m0, s52
	v_lshl_add_u64 v[226:227], s[42:43], 0, v[226:227]
	ds_read_b128 v[168:171], v244 offset:32768
	ds_read_b128 v[172:175], v244 offset:33792
	ds_read_b128 v[176:179], v244 offset:34816
	ds_read_b128 v[180:183], v244 offset:35840
	ds_read_b128 v[184:187], v244 offset:36864
	ds_read_b128 v[188:191], v244 offset:37888
	ds_read_b128 v[192:195], v244 offset:38912
	ds_read_b128 v[196:199], v244 offset:39936
	global_load_lds_dwordx4 v[226:227], off
	v_lshl_add_u64 v[224:225], s[42:43], 0, v[224:225]
	s_mov_b32 m0, s53
	s_nop 0
	global_load_lds_dwordx4 v[224:225], off
	s_waitcnt vmcnt(8)
	s_waitcnt lgkmcnt(0)
	s_barrier
	s_setprio 1
	s_waitcnt lgkmcnt(0)
	v_mfma_f32_16x16x32_bf16 v[132:135], v[136:139], v[168:171], v[132:135]
	v_mfma_f32_16x16x32_bf16 v[128:131], v[144:147], v[168:171], v[128:131]
	v_mfma_f32_16x16x32_bf16 v[124:127], v[136:139], v[176:179], v[124:127]
	v_mfma_f32_16x16x32_bf16 v[120:123], v[144:147], v[176:179], v[120:123]
	v_mfma_f32_16x16x32_bf16 v[108:111], v[136:139], v[184:187], v[108:111]
	v_mfma_f32_16x16x32_bf16 v[104:107], v[144:147], v[184:187], v[104:107]
	v_mfma_f32_16x16x32_bf16 v[92:95], v[136:139], v[192:195], v[92:95]
	v_mfma_f32_16x16x32_bf16 v[88:91], v[144:147], v[192:195], v[88:91]
	v_mfma_f32_16x16x32_bf16 v[132:135], v[140:143], v[172:175], v[132:135]
	v_mfma_f32_16x16x32_bf16 v[128:131], v[148:151], v[172:175], v[128:131]
	v_mfma_f32_16x16x32_bf16 v[124:127], v[140:143], v[180:183], v[124:127]
	v_mfma_f32_16x16x32_bf16 v[120:123], v[148:151], v[180:183], v[120:123]
	v_mfma_f32_16x16x32_bf16 v[108:111], v[140:143], v[188:191], v[108:111]
	v_mfma_f32_16x16x32_bf16 v[104:107], v[148:151], v[188:191], v[104:107]
	v_mfma_f32_16x16x32_bf16 v[92:95], v[140:143], v[196:199], v[92:95]
	v_mfma_f32_16x16x32_bf16 v[88:91], v[148:151], v[196:199], v[88:91]
	s_setprio 0
	s_setprio 1
	v_mfma_f32_16x16x32_bf16 v[116:119], v[152:155], v[168:171], v[116:119]
	v_mfma_f32_16x16x32_bf16 v[112:115], v[160:163], v[168:171], v[112:115]
	v_mfma_f32_16x16x32_bf16 v[100:103], v[152:155], v[176:179], v[100:103]
	v_mfma_f32_16x16x32_bf16 v[96:99], v[160:163], v[176:179], v[96:99]
	v_mfma_f32_16x16x32_bf16 v[80:83], v[152:155], v[184:187], v[80:83]
	v_mfma_f32_16x16x32_bf16 v[76:79], v[160:163], v[184:187], v[76:79]
	v_mfma_f32_16x16x32_bf16 v[72:75], v[152:155], v[192:195], v[72:75]
	v_mfma_f32_16x16x32_bf16 v[68:71], v[160:163], v[192:195], v[68:71]
	v_mfma_f32_16x16x32_bf16 v[116:119], v[156:159], v[172:175], v[116:119]
	v_mfma_f32_16x16x32_bf16 v[112:115], v[164:167], v[172:175], v[112:115]
	v_mfma_f32_16x16x32_bf16 v[100:103], v[156:159], v[180:183], v[100:103]
	v_mfma_f32_16x16x32_bf16 v[96:99], v[164:167], v[180:183], v[96:99]
	v_mfma_f32_16x16x32_bf16 v[80:83], v[156:159], v[188:191], v[80:83]
	v_mfma_f32_16x16x32_bf16 v[76:79], v[164:167], v[188:191], v[76:79]
	v_mfma_f32_16x16x32_bf16 v[72:75], v[156:159], v[196:199], v[72:75]
	v_mfma_f32_16x16x32_bf16 v[68:71], v[164:167], v[196:199], v[68:71]
	s_setprio 0
	s_barrier
	s_add_i32 s42, s62, s44
	v_lshl_add_u64 v[224:225], s[40:41], 0, v[210:211]
	s_mov_b32 m0, s42
	ds_read_b128 v[168:171], v244 offset:49152
	ds_read_b128 v[172:175], v244 offset:50176
	ds_read_b128 v[176:179], v244 offset:51200
	ds_read_b128 v[180:183], v244 offset:52224
	ds_read_b128 v[184:187], v244 offset:53248
	ds_read_b128 v[188:191], v244 offset:54272
	ds_read_b128 v[192:195], v244 offset:55296
	ds_read_b128 v[196:199], v244 offset:56320
	global_load_lds_dwordx4 v[224:225], off
	s_add_i32 m0, s42, 0x2000
	s_add_u32 s38, s38, 0xc000
	v_lshl_add_u64 v[224:225], s[40:41], 0, v[208:209]
	s_addc_u32 s39, s39, 0
	s_add_i32 s40, s63, s44
	global_load_lds_dwordx4 v[224:225], off
	v_lshl_add_u64 v[224:225], s[38:39], 0, v[210:211]
	s_mov_b32 m0, s40
	v_lshl_add_u64 v[204:205], v[204:205], 0, s[36:37]
	global_load_lds_dwordx4 v[224:225], off
	v_lshl_add_u64 v[224:225], s[38:39], 0, v[208:209]
	s_add_i32 m0, s40, 0x2000
	s_nop 0
	global_load_lds_dwordx4 v[224:225], off
	v_lshl_add_u64 v[224:225], v[248:249], 0, s[36:37]
	s_mov_b32 m0, s54
	s_nop 0
	global_load_lds_dwordx4 v[224:225], off
	s_mov_b32 m0, s55
	s_nop 0
	global_load_lds_dwordx4 v[204:205], off
	s_waitcnt vmcnt(8)
	s_waitcnt lgkmcnt(0)
	s_barrier
	s_setprio 1
	s_waitcnt lgkmcnt(0)
	v_mfma_f32_16x16x32_bf16 v[64:67], v[136:139], v[168:171], v[64:67]
	v_mfma_f32_16x16x32_bf16 v[60:63], v[144:147], v[168:171], v[60:63]
	v_mfma_f32_16x16x32_bf16 v[56:59], v[136:139], v[176:179], v[56:59]
	v_mfma_f32_16x16x32_bf16 v[52:55], v[144:147], v[176:179], v[52:55]
	v_mfma_f32_16x16x32_bf16 v[40:43], v[136:139], v[184:187], v[40:43]
	v_mfma_f32_16x16x32_bf16 v[36:39], v[144:147], v[184:187], v[36:39]
	v_mfma_f32_16x16x32_bf16 v[24:27], v[136:139], v[192:195], v[24:27]
	v_mfma_f32_16x16x32_bf16 v[20:23], v[144:147], v[192:195], v[20:23]
	v_mfma_f32_16x16x32_bf16 v[64:67], v[140:143], v[172:175], v[64:67]
	v_mfma_f32_16x16x32_bf16 v[60:63], v[148:151], v[172:175], v[60:63]
	v_mfma_f32_16x16x32_bf16 v[56:59], v[140:143], v[180:183], v[56:59]
	v_mfma_f32_16x16x32_bf16 v[52:55], v[148:151], v[180:183], v[52:55]
	v_mfma_f32_16x16x32_bf16 v[40:43], v[140:143], v[188:191], v[40:43]
	v_mfma_f32_16x16x32_bf16 v[36:39], v[148:151], v[188:191], v[36:39]
	v_mfma_f32_16x16x32_bf16 v[24:27], v[140:143], v[196:199], v[24:27]
	v_mfma_f32_16x16x32_bf16 v[20:23], v[148:151], v[196:199], v[20:23]
	s_setprio 0
	s_setprio 1
	v_mfma_f32_16x16x32_bf16 v[48:51], v[152:155], v[168:171], v[48:51]
	v_mfma_f32_16x16x32_bf16 v[44:47], v[160:163], v[168:171], v[44:47]
	v_mfma_f32_16x16x32_bf16 v[32:35], v[152:155], v[176:179], v[32:35]
	v_mfma_f32_16x16x32_bf16 v[28:31], v[160:163], v[176:179], v[28:31]
	v_mfma_f32_16x16x32_bf16 v[16:19], v[152:155], v[184:187], v[16:19]
	v_mfma_f32_16x16x32_bf16 v[12:15], v[160:163], v[184:187], v[12:15]
	v_mfma_f32_16x16x32_bf16 v[8:11], v[152:155], v[192:195], v[8:11]
	v_mfma_f32_16x16x32_bf16 v[4:7], v[160:163], v[192:195], v[4:7]
	v_mfma_f32_16x16x32_bf16 v[48:51], v[156:159], v[172:175], v[48:51]
	v_mfma_f32_16x16x32_bf16 v[44:47], v[164:167], v[172:175], v[44:47]
	v_mfma_f32_16x16x32_bf16 v[32:35], v[156:159], v[180:183], v[32:35]
	v_mfma_f32_16x16x32_bf16 v[28:31], v[164:167], v[180:183], v[28:31]
	v_mfma_f32_16x16x32_bf16 v[16:19], v[156:159], v[188:191], v[16:19]
	v_mfma_f32_16x16x32_bf16 v[12:15], v[164:167], v[188:191], v[12:15]
	v_mfma_f32_16x16x32_bf16 v[8:11], v[156:159], v[196:199], v[8:11]
	v_mfma_f32_16x16x32_bf16 v[4:7], v[164:167], v[196:199], v[4:7]
	s_setprio 0
	s_barrier
	s_add_i32 s61, s61, 2
	s_add_u32 s59, s59, 0x10000
	s_addc_u32 s60, s60, 0
	s_add_u32 s14, s14, 0x100
	s_addc_u32 s15, s15, 0
	s_cmp_gt_u32 s61, 29
	s_cbranch_scc1 .LBB0_838

.LBB0_1177:
	s_add_u32 s56, s52, 0x80
	s_addc_u32 s57, s53, 0
	s_and_b64 s[54:55], s[54:55], exec
	s_cselect_b32 s55, s11, s81
	s_cselect_b32 s54, s41, s80
	s_mov_b32 m0, s61
	s_cselect_b32 s57, s23, s57
	s_cselect_b32 s56, s22, s56
	v_lshl_add_u64 v[204:205], s[54:55], 0, v[208:209]
	s_add_u32 s84, s54, 0x4000
	global_load_lds_dwordx4 v[204:205], off
	v_lshl_add_u64 v[204:205], s[54:55], 0, v[210:211]
	s_mov_b32 m0, s62
	s_addc_u32 s85, s55, 0
	global_load_lds_dwordx4 v[204:205], off
	v_lshl_add_u64 v[204:205], s[84:85], 0, v[208:209]
	s_mov_b32 m0, s63
	s_and_b64 vcc, exec, s[4:5]
	global_load_lds_dwordx4 v[204:205], off
	v_lshl_add_u64 v[204:205], s[84:85], 0, v[210:211]
	s_mov_b32 m0, s64
	s_nop 0
	global_load_lds_dwordx4 v[204:205], off
	s_mov_b32 m0, s9
	s_nop 0
	global_load_lds_dwordx4 v2, s[56:57]
	s_waitcnt vmcnt(7)
	s_waitcnt lgkmcnt(0)
	s_barrier
	s_cbranch_vccnz .LBB0_1179
	s_setprio 1
	s_waitcnt lgkmcnt(0)
	v_mfma_f32_16x16x32_bf16 v[64:67], v[152:155], v[180:183], v[64:67]
	v_mfma_f32_16x16x32_bf16 v[60:63], v[160:163], v[180:183], v[60:63]
	v_mfma_f32_16x16x32_bf16 v[56:59], v[152:155], v[176:179], v[56:59]
	v_mfma_f32_16x16x32_bf16 v[52:55], v[160:163], v[176:179], v[52:55]
	v_mfma_f32_16x16x32_bf16 v[48:51], v[152:155], v[172:175], v[48:51]
	v_mfma_f32_16x16x32_bf16 v[44:47], v[160:163], v[172:175], v[44:47]
	v_mfma_f32_16x16x32_bf16 v[40:43], v[152:155], v[168:171], v[40:43]
	v_mfma_f32_16x16x32_bf16 v[36:39], v[160:163], v[168:171], v[36:39]
	v_mfma_f32_16x16x32_bf16 v[64:67], v[156:159], v[196:199], v[64:67]
	v_mfma_f32_16x16x32_bf16 v[60:63], v[164:167], v[196:199], v[60:63]
	v_mfma_f32_16x16x32_bf16 v[56:59], v[156:159], v[192:195], v[56:59]
	v_mfma_f32_16x16x32_bf16 v[52:55], v[164:167], v[192:195], v[52:55]
	v_mfma_f32_16x16x32_bf16 v[48:51], v[156:159], v[188:191], v[48:51]
	v_mfma_f32_16x16x32_bf16 v[44:47], v[164:167], v[188:191], v[44:47]
	v_mfma_f32_16x16x32_bf16 v[40:43], v[156:159], v[184:187], v[40:43]
	v_mfma_f32_16x16x32_bf16 v[36:39], v[164:167], v[184:187], v[36:39]
	s_setprio 0
	s_setprio 1
	v_mfma_f32_16x16x32_bf16 v[32:35], v[136:139], v[180:183], v[32:35]
	v_mfma_f32_16x16x32_bf16 v[28:31], v[144:147], v[180:183], v[28:31]
	v_mfma_f32_16x16x32_bf16 v[24:27], v[136:139], v[176:179], v[24:27]
	v_mfma_f32_16x16x32_bf16 v[20:23], v[144:147], v[176:179], v[20:23]
	v_mfma_f32_16x16x32_bf16 v[16:19], v[136:139], v[172:175], v[16:19]
	v_mfma_f32_16x16x32_bf16 v[12:15], v[144:147], v[172:175], v[12:15]
	v_mfma_f32_16x16x32_bf16 v[8:11], v[136:139], v[168:171], v[8:11]
	v_mfma_f32_16x16x32_bf16 v[4:7], v[144:147], v[168:171], v[4:7]
	v_mfma_f32_16x16x32_bf16 v[32:35], v[140:143], v[196:199], v[32:35]
	v_mfma_f32_16x16x32_bf16 v[28:31], v[148:151], v[196:199], v[28:31]
	v_mfma_f32_16x16x32_bf16 v[24:27], v[140:143], v[192:195], v[24:27]
	v_mfma_f32_16x16x32_bf16 v[20:23], v[148:151], v[192:195], v[20:23]
	v_mfma_f32_16x16x32_bf16 v[16:19], v[140:143], v[188:191], v[16:19]
	v_mfma_f32_16x16x32_bf16 v[12:15], v[148:151], v[188:191], v[12:15]
	v_mfma_f32_16x16x32_bf16 v[8:11], v[140:143], v[184:187], v[8:11]
	v_mfma_f32_16x16x32_bf16 v[4:7], v[148:151], v[184:187], v[4:7]
	s_setprio 0
.LBB0_1179:
	s_barrier
	s_mov_b32 m0, s65
	s_nop 0
	global_load_lds_dwordx4 v212, s[56:57]
	v_add_u32_e32 v136, 0x18000, v224
	v_add_u32_e32 v148, 0x1c000, v224
	ds_read_b128 v[152:155], v136
	ds_read_b128 v[156:159], v136 offset:1024
	ds_read_b128 v[160:163], v136 offset:2048
	ds_read_b128 v[164:167], v136 offset:3072
	ds_read_b128 v[136:139], v148
	ds_read_b128 v[140:143], v148 offset:1024
	ds_read_b128 v[144:147], v148 offset:2048
	ds_read_b128 v[148:151], v148 offset:3072
	s_mov_b32 m0, s66
	ds_read_b128 v[180:183], v225 offset:32768
	ds_read_b128 v[196:199], v225 offset:33792
	ds_read_b128 v[176:179], v225 offset:34816
	ds_read_b128 v[192:195], v225 offset:35840
	ds_read_b128 v[172:175], v225 offset:36864
	ds_read_b128 v[188:191], v225 offset:37888
	ds_read_b128 v[168:171], v225 offset:38912
	ds_read_b128 v[184:187], v225 offset:39936
	global_load_lds_dwordx4 v218, s[56:57]
	s_mov_b32 m0, s67
	s_nop 0
	global_load_lds_dwordx4 v220, s[56:57]
	s_waitcnt vmcnt(8)
	s_waitcnt lgkmcnt(0)
	s_barrier
	s_setprio 1
	s_waitcnt lgkmcnt(0)
	v_mfma_f32_16x16x32_bf16 v[132:135], v[152:155], v[180:183], v[132:135]
	v_mfma_f32_16x16x32_bf16 v[128:131], v[160:163], v[180:183], v[128:131]
	v_mfma_f32_16x16x32_bf16 v[124:127], v[152:155], v[176:179], v[124:127]
	v_mfma_f32_16x16x32_bf16 v[120:123], v[160:163], v[176:179], v[120:123]
	v_mfma_f32_16x16x32_bf16 v[116:119], v[152:155], v[172:175], v[116:119]
	v_mfma_f32_16x16x32_bf16 v[112:115], v[160:163], v[172:175], v[112:115]
	v_mfma_f32_16x16x32_bf16 v[108:111], v[152:155], v[168:171], v[108:111]
	v_mfma_f32_16x16x32_bf16 v[104:107], v[160:163], v[168:171], v[104:107]
	v_mfma_f32_16x16x32_bf16 v[132:135], v[156:159], v[196:199], v[132:135]
	v_mfma_f32_16x16x32_bf16 v[128:131], v[164:167], v[196:199], v[128:131]
	v_mfma_f32_16x16x32_bf16 v[124:127], v[156:159], v[192:195], v[124:127]
	v_mfma_f32_16x16x32_bf16 v[120:123], v[164:167], v[192:195], v[120:123]
	v_mfma_f32_16x16x32_bf16 v[116:119], v[156:159], v[188:191], v[116:119]
	v_mfma_f32_16x16x32_bf16 v[112:115], v[164:167], v[188:191], v[112:115]
	v_mfma_f32_16x16x32_bf16 v[108:111], v[156:159], v[184:187], v[108:111]
	v_mfma_f32_16x16x32_bf16 v[104:107], v[164:167], v[184:187], v[104:107]
	s_setprio 0
	s_setprio 1
	v_mfma_f32_16x16x32_bf16 v[100:103], v[136:139], v[180:183], v[100:103]
	v_mfma_f32_16x16x32_bf16 v[96:99], v[144:147], v[180:183], v[96:99]
	v_mfma_f32_16x16x32_bf16 v[92:95], v[136:139], v[176:179], v[92:95]
	v_mfma_f32_16x16x32_bf16 v[88:91], v[144:147], v[176:179], v[88:91]
	v_mfma_f32_16x16x32_bf16 v[80:83], v[136:139], v[172:175], v[80:83]
	v_mfma_f32_16x16x32_bf16 v[76:79], v[144:147], v[172:175], v[76:79]
	v_mfma_f32_16x16x32_bf16 v[72:75], v[136:139], v[168:171], v[72:75]
	v_mfma_f32_16x16x32_bf16 v[68:71], v[144:147], v[168:171], v[68:71]
	v_mfma_f32_16x16x32_bf16 v[100:103], v[140:143], v[196:199], v[100:103]
	v_mfma_f32_16x16x32_bf16 v[96:99], v[148:151], v[196:199], v[96:99]
	v_mfma_f32_16x16x32_bf16 v[92:95], v[140:143], v[192:195], v[92:95]
	v_mfma_f32_16x16x32_bf16 v[88:91], v[148:151], v[192:195], v[88:91]
	v_mfma_f32_16x16x32_bf16 v[80:83], v[140:143], v[188:191], v[80:83]
	v_mfma_f32_16x16x32_bf16 v[76:79], v[148:151], v[188:191], v[76:79]
	v_mfma_f32_16x16x32_bf16 v[72:75], v[140:143], v[184:187], v[72:75]
	v_mfma_f32_16x16x32_bf16 v[68:71], v[148:151], v[184:187], v[68:71]
	s_setprio 0
	s_barrier
	s_and_b64 vcc, exec, s[4:5]
	s_cbranch_vccnz .LBB0_1181
	ds_read_b128 v[180:183], v225 offset:49152
	ds_read_b128 v[196:199], v225 offset:50176
	ds_read_b128 v[176:179], v225 offset:51200
	ds_read_b128 v[192:195], v225 offset:52224
	ds_read_b128 v[172:175], v225 offset:53248
	ds_read_b128 v[188:191], v225 offset:54272
	ds_read_b128 v[168:171], v225 offset:55296
	ds_read_b128 v[184:187], v225 offset:56320

.LBB0_1313:
	s_add_u32 s56, s52, 0x80
	s_addc_u32 s57, s53, 0
	s_and_b64 s[54:55], s[54:55], exec
	s_cselect_b32 s55, s41, s83
	s_cselect_b32 s54, s43, s82
	s_mov_b32 m0, s65
	s_cselect_b32 s57, s25, s57
	s_cselect_b32 s56, s24, s56
	v_lshl_add_u64 v[204:205], s[54:55], 0, v[208:209]
	s_add_u32 s86, s54, 0x4000
	global_load_lds_dwordx4 v[204:205], off
	v_lshl_add_u64 v[204:205], s[54:55], 0, v[210:211]
	s_mov_b32 m0, s66
	s_addc_u32 s87, s55, 0
	global_load_lds_dwordx4 v[204:205], off
	v_lshl_add_u64 v[204:205], s[86:87], 0, v[208:209]
	s_mov_b32 m0, s67
	s_and_b64 vcc, exec, s[4:5]
	global_load_lds_dwordx4 v[204:205], off
	v_lshl_add_u64 v[204:205], s[86:87], 0, v[210:211]
	s_mov_b32 m0, s68
	s_nop 0
	global_load_lds_dwordx4 v[204:205], off
	s_mov_b32 m0, s11
	s_nop 0
	global_load_lds_dwordx4 v2, s[56:57]
	s_waitcnt vmcnt(7)
	s_waitcnt lgkmcnt(0)
	s_barrier
	s_cbranch_vccnz .LBB0_1315
	s_setprio 1
	s_waitcnt lgkmcnt(0)
	v_mfma_f32_16x16x32_bf16 v[64:67], v[152:155], v[180:183], v[64:67]
	v_mfma_f32_16x16x32_bf16 v[60:63], v[160:163], v[180:183], v[60:63]
	v_mfma_f32_16x16x32_bf16 v[56:59], v[152:155], v[176:179], v[56:59]
	v_mfma_f32_16x16x32_bf16 v[52:55], v[160:163], v[176:179], v[52:55]
	v_mfma_f32_16x16x32_bf16 v[48:51], v[152:155], v[172:175], v[48:51]
	v_mfma_f32_16x16x32_bf16 v[44:47], v[160:163], v[172:175], v[44:47]
	v_mfma_f32_16x16x32_bf16 v[40:43], v[152:155], v[168:171], v[40:43]
	v_mfma_f32_16x16x32_bf16 v[36:39], v[160:163], v[168:171], v[36:39]
	v_mfma_f32_16x16x32_bf16 v[64:67], v[156:159], v[196:199], v[64:67]
	v_mfma_f32_16x16x32_bf16 v[60:63], v[164:167], v[196:199], v[60:63]
	v_mfma_f32_16x16x32_bf16 v[56:59], v[156:159], v[192:195], v[56:59]
	v_mfma_f32_16x16x32_bf16 v[52:55], v[164:167], v[192:195], v[52:55]
	v_mfma_f32_16x16x32_bf16 v[48:51], v[156:159], v[188:191], v[48:51]
	v_mfma_f32_16x16x32_bf16 v[44:47], v[164:167], v[188:191], v[44:47]
	v_mfma_f32_16x16x32_bf16 v[40:43], v[156:159], v[184:187], v[40:43]
	v_mfma_f32_16x16x32_bf16 v[36:39], v[164:167], v[184:187], v[36:39]
	s_setprio 0
	s_setprio 1
	v_mfma_f32_16x16x32_bf16 v[32:35], v[136:139], v[180:183], v[32:35]
	v_mfma_f32_16x16x32_bf16 v[28:31], v[144:147], v[180:183], v[28:31]
	v_mfma_f32_16x16x32_bf16 v[24:27], v[136:139], v[176:179], v[24:27]
	v_mfma_f32_16x16x32_bf16 v[20:23], v[144:147], v[176:179], v[20:23]
	v_mfma_f32_16x16x32_bf16 v[16:19], v[136:139], v[172:175], v[16:19]
	v_mfma_f32_16x16x32_bf16 v[12:15], v[144:147], v[172:175], v[12:15]
	v_mfma_f32_16x16x32_bf16 v[8:11], v[136:139], v[168:171], v[8:11]
	v_mfma_f32_16x16x32_bf16 v[4:7], v[144:147], v[168:171], v[4:7]
	v_mfma_f32_16x16x32_bf16 v[32:35], v[140:143], v[196:199], v[32:35]
	v_mfma_f32_16x16x32_bf16 v[28:31], v[148:151], v[196:199], v[28:31]
	v_mfma_f32_16x16x32_bf16 v[24:27], v[140:143], v[192:195], v[24:27]
	v_mfma_f32_16x16x32_bf16 v[20:23], v[148:151], v[192:195], v[20:23]
	v_mfma_f32_16x16x32_bf16 v[16:19], v[140:143], v[188:191], v[16:19]
	v_mfma_f32_16x16x32_bf16 v[12:15], v[148:151], v[188:191], v[12:15]
	v_mfma_f32_16x16x32_bf16 v[8:11], v[140:143], v[184:187], v[8:11]
	v_mfma_f32_16x16x32_bf16 v[4:7], v[148:151], v[184:187], v[4:7]
	s_setprio 0
.LBB0_1315:
	s_barrier
	s_mov_b32 m0, s69
	s_nop 0
	global_load_lds_dwordx4 v212, s[56:57]
	v_add_u32_e32 v136, 0x18000, v241
	v_add_u32_e32 v148, 0x1c000, v241
	ds_read_b128 v[152:155], v136
	ds_read_b128 v[156:159], v136 offset:1024
	ds_read_b128 v[160:163], v136 offset:2048
	ds_read_b128 v[164:167], v136 offset:3072
	ds_read_b128 v[136:139], v148
	ds_read_b128 v[140:143], v148 offset:1024
	ds_read_b128 v[144:147], v148 offset:2048
	ds_read_b128 v[148:151], v148 offset:3072
	s_mov_b32 m0, s70
	ds_read_b128 v[180:183], v242 offset:32768
	ds_read_b128 v[196:199], v242 offset:33792
	ds_read_b128 v[176:179], v242 offset:34816
	ds_read_b128 v[192:195], v242 offset:35840
	ds_read_b128 v[172:175], v242 offset:36864
	ds_read_b128 v[188:191], v242 offset:37888
	ds_read_b128 v[168:171], v242 offset:38912
	ds_read_b128 v[184:187], v242 offset:39936
	global_load_lds_dwordx4 v218, s[56:57]
	s_mov_b32 m0, s71
	s_nop 0
	global_load_lds_dwordx4 v219, s[56:57]
	s_waitcnt vmcnt(8)
	s_waitcnt lgkmcnt(0)
	s_barrier
	s_setprio 1
	s_waitcnt lgkmcnt(0)
	v_mfma_f32_16x16x32_bf16 v[132:135], v[152:155], v[180:183], v[132:135]
	v_mfma_f32_16x16x32_bf16 v[128:131], v[160:163], v[180:183], v[128:131]
	v_mfma_f32_16x16x32_bf16 v[124:127], v[152:155], v[176:179], v[124:127]
	v_mfma_f32_16x16x32_bf16 v[120:123], v[160:163], v[176:179], v[120:123]
	v_mfma_f32_16x16x32_bf16 v[116:119], v[152:155], v[172:175], v[116:119]
	v_mfma_f32_16x16x32_bf16 v[112:115], v[160:163], v[172:175], v[112:115]
	v_mfma_f32_16x16x32_bf16 v[108:111], v[152:155], v[168:171], v[108:111]
	v_mfma_f32_16x16x32_bf16 v[104:107], v[160:163], v[168:171], v[104:107]
	v_mfma_f32_16x16x32_bf16 v[132:135], v[156:159], v[196:199], v[132:135]
	v_mfma_f32_16x16x32_bf16 v[128:131], v[164:167], v[196:199], v[128:131]
	v_mfma_f32_16x16x32_bf16 v[124:127], v[156:159], v[192:195], v[124:127]
	v_mfma_f32_16x16x32_bf16 v[120:123], v[164:167], v[192:195], v[120:123]
	v_mfma_f32_16x16x32_bf16 v[116:119], v[156:159], v[188:191], v[116:119]
	v_mfma_f32_16x16x32_bf16 v[112:115], v[164:167], v[188:191], v[112:115]
	v_mfma_f32_16x16x32_bf16 v[108:111], v[156:159], v[184:187], v[108:111]
	v_mfma_f32_16x16x32_bf16 v[104:107], v[164:167], v[184:187], v[104:107]
	s_setprio 0
	s_setprio 1
	v_mfma_f32_16x16x32_bf16 v[100:103], v[136:139], v[180:183], v[100:103]
	v_mfma_f32_16x16x32_bf16 v[96:99], v[144:147], v[180:183], v[96:99]
	v_mfma_f32_16x16x32_bf16 v[92:95], v[136:139], v[176:179], v[92:95]
	v_mfma_f32_16x16x32_bf16 v[88:91], v[144:147], v[176:179], v[88:91]
	v_mfma_f32_16x16x32_bf16 v[80:83], v[136:139], v[172:175], v[80:83]
	v_mfma_f32_16x16x32_bf16 v[76:79], v[144:147], v[172:175], v[76:79]
	v_mfma_f32_16x16x32_bf16 v[72:75], v[136:139], v[168:171], v[72:75]
	v_mfma_f32_16x16x32_bf16 v[68:71], v[144:147], v[168:171], v[68:71]
	v_mfma_f32_16x16x32_bf16 v[100:103], v[140:143], v[196:199], v[100:103]
	v_mfma_f32_16x16x32_bf16 v[96:99], v[148:151], v[196:199], v[96:99]
	v_mfma_f32_16x16x32_bf16 v[92:95], v[140:143], v[192:195], v[92:95]
	v_mfma_f32_16x16x32_bf16 v[88:91], v[148:151], v[192:195], v[88:91]
	v_mfma_f32_16x16x32_bf16 v[80:83], v[140:143], v[188:191], v[80:83]
	v_mfma_f32_16x16x32_bf16 v[76:79], v[148:151], v[188:191], v[76:79]
	v_mfma_f32_16x16x32_bf16 v[72:75], v[140:143], v[184:187], v[72:75]
	v_mfma_f32_16x16x32_bf16 v[68:71], v[148:151], v[184:187], v[68:71]
	s_setprio 0
	s_barrier
	s_and_b64 vcc, exec, s[4:5]
	s_cbranch_vccnz .LBB0_1317
	ds_read_b128 v[180:183], v242 offset:49152
	ds_read_b128 v[196:199], v242 offset:50176
	ds_read_b128 v[176:179], v242 offset:51200
	ds_read_b128 v[192:195], v242 offset:52224
	ds_read_b128 v[172:175], v242 offset:53248
	ds_read_b128 v[188:191], v242 offset:54272
	ds_read_b128 v[168:171], v242 offset:55296
	ds_read_b128 v[184:187], v242 offset:56320

.LBB0_1429:
	s_add_u32 s52, s48, 0x80
	s_addc_u32 s53, s49, 0
	s_and_b64 s[50:51], s[50:51], exec
	s_cselect_b32 s51, s15, s74
	s_cselect_b32 s50, s39, s73
	s_mov_b32 m0, s55
	s_cselect_b32 s53, s25, s53
	s_cselect_b32 s52, s24, s52
	v_lshl_add_u64 v[200:201], s[50:51], 0, v[208:209]
	s_add_u32 s76, s50, 0x4000
	global_load_lds_dwordx4 v[200:201], off
	v_lshl_add_u64 v[200:201], s[50:51], 0, v[210:211]
	s_mov_b32 m0, s56
	s_addc_u32 s77, s51, 0
	global_load_lds_dwordx4 v[200:201], off
	v_lshl_add_u64 v[200:201], s[76:77], 0, v[208:209]
	s_mov_b32 m0, s57
	s_and_b64 vcc, exec, s[4:5]
	global_load_lds_dwordx4 v[200:201], off
	v_lshl_add_u64 v[200:201], s[76:77], 0, v[210:211]
	s_mov_b32 m0, s59
	s_nop 0
	global_load_lds_dwordx4 v[200:201], off
	s_mov_b32 m0, s7
	s_nop 0
	global_load_lds_dwordx4 v2, s[52:53]
	s_waitcnt vmcnt(7)
	s_waitcnt lgkmcnt(0)
	s_barrier
	s_cbranch_vccnz .LBB0_1431
	s_setprio 1
	s_waitcnt lgkmcnt(0)
	v_mfma_f32_16x16x32_bf16 v[64:67], v[152:155], v[180:183], v[64:67]
	v_mfma_f32_16x16x32_bf16 v[60:63], v[160:163], v[180:183], v[60:63]
	v_mfma_f32_16x16x32_bf16 v[56:59], v[152:155], v[176:179], v[56:59]
	v_mfma_f32_16x16x32_bf16 v[52:55], v[160:163], v[176:179], v[52:55]
	v_mfma_f32_16x16x32_bf16 v[48:51], v[152:155], v[172:175], v[48:51]
	v_mfma_f32_16x16x32_bf16 v[44:47], v[160:163], v[172:175], v[44:47]
	v_mfma_f32_16x16x32_bf16 v[40:43], v[152:155], v[168:171], v[40:43]
	v_mfma_f32_16x16x32_bf16 v[36:39], v[160:163], v[168:171], v[36:39]
	v_mfma_f32_16x16x32_bf16 v[64:67], v[156:159], v[196:199], v[64:67]
	v_mfma_f32_16x16x32_bf16 v[60:63], v[164:167], v[196:199], v[60:63]
	v_mfma_f32_16x16x32_bf16 v[56:59], v[156:159], v[192:195], v[56:59]
	v_mfma_f32_16x16x32_bf16 v[52:55], v[164:167], v[192:195], v[52:55]
	v_mfma_f32_16x16x32_bf16 v[48:51], v[156:159], v[188:191], v[48:51]
	v_mfma_f32_16x16x32_bf16 v[44:47], v[164:167], v[188:191], v[44:47]
	v_mfma_f32_16x16x32_bf16 v[40:43], v[156:159], v[184:187], v[40:43]
	v_mfma_f32_16x16x32_bf16 v[36:39], v[164:167], v[184:187], v[36:39]
	s_setprio 0
	s_setprio 1
	v_mfma_f32_16x16x32_bf16 v[32:35], v[136:139], v[180:183], v[32:35]
	v_mfma_f32_16x16x32_bf16 v[28:31], v[144:147], v[180:183], v[28:31]
	v_mfma_f32_16x16x32_bf16 v[24:27], v[136:139], v[176:179], v[24:27]
	v_mfma_f32_16x16x32_bf16 v[20:23], v[144:147], v[176:179], v[20:23]
	v_mfma_f32_16x16x32_bf16 v[16:19], v[136:139], v[172:175], v[16:19]
	v_mfma_f32_16x16x32_bf16 v[12:15], v[144:147], v[172:175], v[12:15]
	v_mfma_f32_16x16x32_bf16 v[8:11], v[136:139], v[168:171], v[8:11]
	v_mfma_f32_16x16x32_bf16 v[4:7], v[144:147], v[168:171], v[4:7]
	v_mfma_f32_16x16x32_bf16 v[32:35], v[140:143], v[196:199], v[32:35]
	v_mfma_f32_16x16x32_bf16 v[28:31], v[148:151], v[196:199], v[28:31]
	v_mfma_f32_16x16x32_bf16 v[24:27], v[140:143], v[192:195], v[24:27]
	v_mfma_f32_16x16x32_bf16 v[20:23], v[148:151], v[192:195], v[20:23]
	v_mfma_f32_16x16x32_bf16 v[16:19], v[140:143], v[188:191], v[16:19]
	v_mfma_f32_16x16x32_bf16 v[12:15], v[148:151], v[188:191], v[12:15]
	v_mfma_f32_16x16x32_bf16 v[8:11], v[140:143], v[184:187], v[8:11]
	v_mfma_f32_16x16x32_bf16 v[4:7], v[148:151], v[184:187], v[4:7]
	s_setprio 0
.LBB0_1431:
	s_barrier
	s_mov_b32 m0, s60
	s_nop 0
	global_load_lds_dwordx4 v212, s[52:53]
	v_add_u32_e32 v136, 0x18000, v241
	v_add_u32_e32 v148, 0x1c000, v241
	ds_read_b128 v[152:155], v136
	ds_read_b128 v[156:159], v136 offset:1024
	ds_read_b128 v[160:163], v136 offset:2048
	ds_read_b128 v[164:167], v136 offset:3072
	ds_read_b128 v[136:139], v148
	ds_read_b128 v[140:143], v148 offset:1024
	ds_read_b128 v[144:147], v148 offset:2048
	ds_read_b128 v[148:151], v148 offset:3072
	s_mov_b32 m0, s61
	ds_read_b128 v[180:183], v242 offset:32768
	ds_read_b128 v[196:199], v242 offset:33792
	ds_read_b128 v[176:179], v242 offset:34816
	ds_read_b128 v[192:195], v242 offset:35840
	ds_read_b128 v[172:175], v242 offset:36864
	ds_read_b128 v[188:191], v242 offset:37888
	ds_read_b128 v[168:171], v242 offset:38912
	ds_read_b128 v[184:187], v242 offset:39936
	global_load_lds_dwordx4 v218, s[52:53]
	s_mov_b32 m0, s62
	s_nop 0
	global_load_lds_dwordx4 v219, s[52:53]
	s_waitcnt vmcnt(8)
	s_waitcnt lgkmcnt(0)
	s_barrier
	s_setprio 1
	s_waitcnt lgkmcnt(0)
	v_mfma_f32_16x16x32_bf16 v[132:135], v[152:155], v[180:183], v[132:135]
	v_mfma_f32_16x16x32_bf16 v[128:131], v[160:163], v[180:183], v[128:131]
	v_mfma_f32_16x16x32_bf16 v[124:127], v[152:155], v[176:179], v[124:127]
	v_mfma_f32_16x16x32_bf16 v[120:123], v[160:163], v[176:179], v[120:123]
	v_mfma_f32_16x16x32_bf16 v[116:119], v[152:155], v[172:175], v[116:119]
	v_mfma_f32_16x16x32_bf16 v[112:115], v[160:163], v[172:175], v[112:115]
	v_mfma_f32_16x16x32_bf16 v[108:111], v[152:155], v[168:171], v[108:111]
	v_mfma_f32_16x16x32_bf16 v[104:107], v[160:163], v[168:171], v[104:107]
	v_mfma_f32_16x16x32_bf16 v[132:135], v[156:159], v[196:199], v[132:135]
	v_mfma_f32_16x16x32_bf16 v[128:131], v[164:167], v[196:199], v[128:131]
	v_mfma_f32_16x16x32_bf16 v[124:127], v[156:159], v[192:195], v[124:127]
	v_mfma_f32_16x16x32_bf16 v[120:123], v[164:167], v[192:195], v[120:123]
	v_mfma_f32_16x16x32_bf16 v[116:119], v[156:159], v[188:191], v[116:119]
	v_mfma_f32_16x16x32_bf16 v[112:115], v[164:167], v[188:191], v[112:115]
	v_mfma_f32_16x16x32_bf16 v[108:111], v[156:159], v[184:187], v[108:111]
	v_mfma_f32_16x16x32_bf16 v[104:107], v[164:167], v[184:187], v[104:107]
	s_setprio 0
	s_setprio 1
	v_mfma_f32_16x16x32_bf16 v[100:103], v[136:139], v[180:183], v[100:103]
	v_mfma_f32_16x16x32_bf16 v[96:99], v[144:147], v[180:183], v[96:99]
	v_mfma_f32_16x16x32_bf16 v[92:95], v[136:139], v[176:179], v[92:95]
	v_mfma_f32_16x16x32_bf16 v[88:91], v[144:147], v[176:179], v[88:91]
	v_mfma_f32_16x16x32_bf16 v[80:83], v[136:139], v[172:175], v[80:83]
	v_mfma_f32_16x16x32_bf16 v[76:79], v[144:147], v[172:175], v[76:79]
	v_mfma_f32_16x16x32_bf16 v[72:75], v[136:139], v[168:171], v[72:75]
	v_mfma_f32_16x16x32_bf16 v[68:71], v[144:147], v[168:171], v[68:71]
	v_mfma_f32_16x16x32_bf16 v[100:103], v[140:143], v[196:199], v[100:103]
	v_mfma_f32_16x16x32_bf16 v[96:99], v[148:151], v[196:199], v[96:99]
	v_mfma_f32_16x16x32_bf16 v[92:95], v[140:143], v[192:195], v[92:95]
	v_mfma_f32_16x16x32_bf16 v[88:91], v[148:151], v[192:195], v[88:91]
	v_mfma_f32_16x16x32_bf16 v[80:83], v[140:143], v[188:191], v[80:83]
	v_mfma_f32_16x16x32_bf16 v[76:79], v[148:151], v[188:191], v[76:79]
	v_mfma_f32_16x16x32_bf16 v[72:75], v[140:143], v[184:187], v[72:75]
	v_mfma_f32_16x16x32_bf16 v[68:71], v[148:151], v[184:187], v[68:71]
	s_setprio 0
	s_barrier
	s_and_b64 vcc, exec, s[4:5]
	s_cbranch_vccnz .LBB0_1433
	ds_read_b128 v[180:183], v242 offset:49152
	ds_read_b128 v[196:199], v242 offset:50176
	ds_read_b128 v[176:179], v242 offset:51200
	ds_read_b128 v[192:195], v242 offset:52224
	ds_read_b128 v[172:175], v242 offset:53248
	ds_read_b128 v[188:191], v242 offset:54272
	ds_read_b128 v[168:171], v242 offset:55296
	ds_read_b128 v[184:187], v242 offset:56320
